# weight-conversion loop: removed a loop-header vmcnt drain that only guards an unreachable path, so both load buffers stay in flight; deeper attention V prefetch
# speedup vs baseline: 1.0152x; 1.0080x over previous
; __device__ __forceinline__ cgptr cuni(const void* p) { const unsigned long long v = (unsigned long long)p; const unsigned lo = __builtin_amdgcn_readfirstlane((unsigned)v), hi = __builtin_amdgcn_readfirstlane((unsigned)(v >> 32)); return (cgptr)(((unsigned long long)hi << 32) | lo); }
; #define CONV_LOAD(v, c) do { const unsigned lo_ = (unsigned)(lane >> 3) * (c).N4 + 16u * (unsigned)(lane & 7); _Pragma("unroll") for (int i = 0; i < 16; ++i) v[i] = __builtin_nontemporal_load((const GAS f32x4*)(cuni((const void*)((c).src + (size_t)(8 * i) * (c).N4)) + lo_)); } while (0)
; __device__ __forceinline__ ConvItem conv_decode(int it, const float* wgu, const float* wd, unsigned char* WguT, unsigned char* WdT) {
;     constexpr int I_GU = NE * 16 * 128;
;     ConvItem c; int r = it, nbn, N; const float* src; unsigned char* dstp; bool gu;
;     if (r < I_GU) { const int e = r / (16 * 128); r -= e * (16 * 128); N = 4096; nbn = 128; src = wgu + (size_t)e * DM * 4096; dstp = WguT + (size_t)e * 4096 * DM; gu = true; }
;     else { r -= I_GU; const int e = r / (16 * 64); r -= e * (16 * 64); N = DM; nbn = 64; src = wd + (size_t)e * DFF * DM; dstp = WdT + (size_t)e * DM * DFF; gu = false; }
;     const int kb = r / nbn, nb = r - kb * nbn, n0 = nb * 32, k0 = kb * 128; int dst = n0;
;     if (gu) { const int j = n0 & 2047; dst = (j >> 7) * 256 + (j & 127) + ((n0 >= 2048) ? 128 : 0); }
;     c.src = cuni(src + (size_t)k0 * N + n0); c.dstp = cuni(dstp + (size_t)dst * DM + k0); c.N4 = (unsigned)N * 4u;
;     return c;
; }
; __device__ __forceinline__ void convert_expert_weights(const float* wgu, const float* wd, unsigned char* WguT, unsigned char* WdT, LAS float* scr, int gw, int NGW, int NIT, int lane) {
;     ...
;         const bool ha = it + NGW < NIT; ca = conv_decode(ha ? it + NGW : it, wgu, wd, WguT, WdT); CONV_LOAD(va, ca);
;         CONV_STORE(vb, cb);
.LBB0_494:
	v_cvt_f32_ubyte0_e32 v64, s10
	v_rcp_iflag_f32_e32 v64, v64
	s_sub_i32 s17, 0, s10
	s_abs_i32 s12, s9
	s_ashr_i32 s11, s9, 31
	v_mul_f32_e32 v64, 0x4f7ffffe, v64
	v_cvt_u32_f32_e32 v64, v64
	v_add_u32_e32 v152, 0x400, v148
	v_add_u32_e32 v153, 0x400, v149
	v_add_u32_e32 v154, 0x400, v150
	v_readfirstlane_b32 s26, v64
	s_mul_i32 s17, s17, s26
	s_mul_hi_u32 s17, s26, s17
	s_add_i32 s26, s26, s17
	s_mul_hi_u32 s17, s12, s26
	s_mul_i32 s26, s17, s10
	s_sub_i32 s12, s12, s26
	s_add_i32 s27, s17, 1
	s_sub_i32 s26, s12, s10
	s_cmp_ge_u32 s12, s10
	s_cselect_b32 s17, s27, s17
	s_cselect_b32 s12, s26, s12
	s_add_i32 s26, s17, 1
	s_cmp_ge_u32 s12, s10
	s_cselect_b32 s12, s26, s17
	s_xor_b32 s12, s12, s11
	s_sub_i32 s11, s12, s11
	s_mul_i32 s10, s11, s10
	s_lshl_b32 s17, s9, 6
	s_sub_i32 s9, s9, s10
	s_lshl_b32 s10, s9, 5
	s_and_b32 s12, s17, 0xf00
	s_and_b32 s17, s10, 0x60
	s_or_b32 s12, s17, s12
	s_cmp_gt_i32 s9, 63
	s_cselect_b32 s9, 0x80, 0
	s_or_b32 s9, s12, s9
	s_and_b64 s[18:19], s[18:19], exec
	s_cselect_b32 s18, s9, s10
	s_lshl_b32 s9, s11, 7
	s_mul_hi_i32 s27, s9, s8
	s_mul_i32 s26, s9, s8
	s_ashr_i32 s12, s9, 31
	s_lshl_b64 s[26:27], s[26:27], 2
	s_add_u32 s17, s24, s26
	s_addc_u32 s19, s25, s27
	s_ashr_i32 s11, s10, 31
	s_lshl_b64 s[10:11], s[10:11], 2
	s_add_u32 s24, s17, s10
	s_addc_u32 s25, s19, s11
	s_ashr_i32 s19, s18, 31
	s_lshl_b64 s[10:11], s[18:19], 11
	s_add_u32 s10, s22, s10
	s_addc_u32 s11, s23, s11
	s_add_u32 s18, s10, s9
	s_addc_u32 s19, s11, s12
	s_lshl_b32 s9, s8, 5
	v_mul_lo_u32 v64, v130, s8
	s_add_u32 s10, s24, s9
	v_or_b32_e32 v64, v64, v131
	s_addc_u32 s11, s25, 0
	s_lshl_b32 s9, s8, 6
	global_load_dwordx4 v[124:127], v64, s[24:25] nt
	global_load_dwordx4 v[116:119], v64, s[10:11] nt
	s_add_u32 s10, s24, s9
	s_addc_u32 s11, s25, 0
	s_mul_i32 s9, s8, 0x60
	s_add_u32 s22, s24, s9
	s_addc_u32 s23, s25, 0
	s_lshl_b32 s9, s8, 7
	global_load_dwordx4 v[120:123], v64, s[10:11] nt
	global_load_dwordx4 v[108:111], v64, s[22:23] nt
	s_add_u32 s10, s24, s9
	s_addc_u32 s11, s25, 0
	s_mul_i32 s9, s8, 0xa0
	s_add_u32 s22, s24, s9
	s_addc_u32 s23, s25, 0
	s_mul_i32 s9, s8, 0xc0
	global_load_dwordx4 v[112:115], v64, s[10:11] nt
	global_load_dwordx4 v[100:103], v64, s[22:23] nt
	s_add_u32 s10, s24, s9
	s_addc_u32 s11, s25, 0
	s_mul_i32 s9, s8, 0xe0
	s_add_u32 s22, s24, s9
	s_addc_u32 s23, s25, 0
	s_lshl_b32 s9, s8, 8
	global_load_dwordx4 v[104:107], v64, s[10:11] nt
	global_load_dwordx4 v[92:95], v64, s[22:23] nt
	s_add_u32 s10, s24, s9
	s_addc_u32 s11, s25, 0
	s_mul_i32 s9, s8, 0x120
	s_add_u32 s22, s24, s9
	s_addc_u32 s23, s25, 0
	s_mul_i32 s9, s8, 0x140
	global_load_dwordx4 v[96:99], v64, s[10:11] nt
	global_load_dwordx4 v[84:87], v64, s[22:23] nt
	s_add_u32 s10, s24, s9
	s_addc_u32 s11, s25, 0
	s_mul_i32 s9, s8, 0x160
	s_add_u32 s22, s24, s9
	s_addc_u32 s23, s25, 0
	s_mul_i32 s9, s8, 0x180
	global_load_dwordx4 v[88:91], v64, s[10:11] nt
	global_load_dwordx4 v[76:79], v64, s[22:23] nt
	s_add_u32 s10, s24, s9
	s_addc_u32 s11, s25, 0
	s_mul_i32 s9, s8, 0x1a0
	s_add_u32 s22, s24, s9
	s_addc_u32 s23, s25, 0
	s_mul_i32 s9, s8, 0x1c0
	global_load_dwordx4 v[80:83], v64, s[10:11] nt
	global_load_dwordx4 v[68:71], v64, s[22:23] nt
	s_add_u32 s10, s24, s9
	s_addc_u32 s11, s25, 0
	s_mulk_i32 s8, 0x1e0
	s_add_u32 s8, s24, s8
	s_waitcnt vmcnt(29)
	v_pk_mul_f32 v[6:7], v[6:7], s[16:17] op_sel_hi:[1,0]
	v_pk_mul_f32 v[4:5], v[4:5], s[16:17] op_sel_hi:[1,0]
	s_waitcnt vmcnt(28)
	v_pk_mul_f32 v[2:3], v[2:3], s[16:17] op_sel_hi:[1,0]
	v_pk_mul_f32 v[0:1], v[0:1], s[16:17] op_sel_hi:[1,0]
	s_addc_u32 s9, s25, 0
	global_load_dwordx4 v[72:75], v64, s[10:11] nt
	s_nop 0
	global_load_dwordx4 v[64:67], v64, s[8:9] nt
	ds_write_b128 v132, v[4:7]
	ds_write_b128 v133, v[0:3]
	s_waitcnt vmcnt(29)
	v_pk_mul_f32 v[2:3], v[14:15], s[16:17] op_sel_hi:[1,0]
	v_pk_mul_f32 v[0:1], v[12:13], s[16:17] op_sel_hi:[1,0]
	ds_write_b128 v134, v[0:3]
	s_waitcnt vmcnt(28)
	v_pk_mul_f32 v[2:3], v[10:11], s[16:17] op_sel_hi:[1,0]
	v_pk_mul_f32 v[0:1], v[8:9], s[16:17] op_sel_hi:[1,0]
	ds_write_b128 v135, v[0:3]
	s_waitcnt vmcnt(27)
	v_pk_mul_f32 v[2:3], v[22:23], s[16:17] op_sel_hi:[1,0]
	v_pk_mul_f32 v[0:1], v[20:21], s[16:17] op_sel_hi:[1,0]
	ds_write_b128 v136, v[0:3]
	s_waitcnt vmcnt(26)
	v_pk_mul_f32 v[2:3], v[18:19], s[16:17] op_sel_hi:[1,0]
	v_pk_mul_f32 v[0:1], v[16:17], s[16:17] op_sel_hi:[1,0]
	ds_write_b128 v137, v[0:3]
	s_waitcnt vmcnt(25)
	v_pk_mul_f32 v[2:3], v[30:31], s[16:17] op_sel_hi:[1,0]
	v_pk_mul_f32 v[0:1], v[28:29], s[16:17] op_sel_hi:[1,0]
	ds_write_b128 v138, v[0:3]
	s_waitcnt vmcnt(24)
	v_pk_mul_f32 v[2:3], v[26:27], s[16:17] op_sel_hi:[1,0]
	v_pk_mul_f32 v[0:1], v[24:25], s[16:17] op_sel_hi:[1,0]
	ds_write_b128 v139, v[0:3]
	s_waitcnt vmcnt(23)
	v_pk_mul_f32 v[2:3], v[38:39], s[16:17] op_sel_hi:[1,0]
	v_pk_mul_f32 v[0:1], v[36:37], s[16:17] op_sel_hi:[1,0]
	ds_write_b128 v140, v[0:3]
	s_waitcnt vmcnt(22)
	v_pk_mul_f32 v[2:3], v[34:35], s[16:17] op_sel_hi:[1,0]
	v_pk_mul_f32 v[0:1], v[32:33], s[16:17] op_sel_hi:[1,0]
	ds_write_b128 v141, v[0:3]
	s_waitcnt vmcnt(21)
	v_pk_mul_f32 v[2:3], v[46:47], s[16:17] op_sel_hi:[1,0]
	v_pk_mul_f32 v[0:1], v[44:45], s[16:17] op_sel_hi:[1,0]
	ds_write_b128 v142, v[0:3]
	s_waitcnt vmcnt(20)
	v_pk_mul_f32 v[2:3], v[42:43], s[16:17] op_sel_hi:[1,0]
	v_pk_mul_f32 v[0:1], v[40:41], s[16:17] op_sel_hi:[1,0]
	ds_write_b128 v143, v[0:3]
	s_waitcnt vmcnt(19)
	v_pk_mul_f32 v[2:3], v[54:55], s[16:17] op_sel_hi:[1,0]
	v_pk_mul_f32 v[0:1], v[52:53], s[16:17] op_sel_hi:[1,0]
	ds_write_b128 v144, v[0:3]
	s_waitcnt vmcnt(18)
	v_pk_mul_f32 v[2:3], v[50:51], s[16:17] op_sel_hi:[1,0]
	v_pk_mul_f32 v[0:1], v[48:49], s[16:17] op_sel_hi:[1,0]
	ds_write_b128 v145, v[0:3]
	s_waitcnt vmcnt(17)
	v_pk_mul_f32 v[2:3], v[62:63], s[16:17] op_sel_hi:[1,0]
	v_pk_mul_f32 v[0:1], v[60:61], s[16:17] op_sel_hi:[1,0]
	ds_write_b128 v146, v[0:3]
	s_waitcnt vmcnt(16)
	v_pk_mul_f32 v[2:3], v[58:59], s[16:17] op_sel_hi:[1,0]
	v_pk_mul_f32 v[0:1], v[56:57], s[16:17] op_sel_hi:[1,0]
	ds_write_b128 v147, v[0:3]
	s_waitcnt lgkmcnt(0)
	ds_read2_b32 v[0:1], v148 offset1:32
	ds_read2_b32 v[8:9], v148 offset0:64 offset1:96
	s_add_u32 s8, s14, 0x4000
	s_waitcnt lgkmcnt(0)
	v_cvt_pk_fp8_f32 v4, v0, v1
	ds_read2_b32 v[0:1], v148 offset0:128 offset1:160
	ds_read2_b32 v[10:11], v148 offset0:192 offset1:224
	ds_read2_b32 v[12:13], v152 offset1:32
	s_waitcnt lgkmcnt(2)
	v_cvt_pk_fp8_f32 v5, v0, v1
	ds_read2_b32 v[0:1], v152 offset0:64 offset1:96
	ds_read2_b32 v[14:15], v152 offset0:128 offset1:160
	s_waitcnt lgkmcnt(2)
	v_cvt_pk_fp8_f32 v6, v12, v13
	ds_read2_b32 v[12:13], v152 offset0:192 offset1:224
	v_cvt_pk_fp8_f32 v4, v8, v9 op_sel:[0,0,1]
	s_waitcnt lgkmcnt(1)
	v_cvt_pk_fp8_f32 v7, v14, v15
	v_cvt_pk_fp8_f32 v5, v10, v11 op_sel:[0,0,1]
	v_cvt_pk_fp8_f32 v6, v0, v1 op_sel:[0,0,1]
	ds_read2_b32 v[0:1], v149 offset1:32
	s_waitcnt lgkmcnt(1)
	v_cvt_pk_fp8_f32 v7, v12, v13 op_sel:[0,0,1]
	v_lshl_add_u64 v[8:9], s[14:15], 0, v[128:129]
	s_addc_u32 s9, s15, 0
	v_add_u32_e32 v155, 0x400, v151
	global_store_dwordx4 v[8:9], v[4:7], off nt
	ds_read2_b32 v[8:9], v149 offset0:64 offset1:96
	s_waitcnt lgkmcnt(1)
	v_cvt_pk_fp8_f32 v4, v0, v1
	ds_read2_b32 v[0:1], v149 offset0:128 offset1:160
	ds_read2_b32 v[10:11], v149 offset0:192 offset1:224
	ds_read2_b32 v[12:13], v153 offset1:32
	s_waitcnt lgkmcnt(2)
	v_cvt_pk_fp8_f32 v5, v0, v1
	ds_read2_b32 v[0:1], v153 offset0:64 offset1:96
	ds_read2_b32 v[14:15], v153 offset0:128 offset1:160
	s_waitcnt lgkmcnt(2)
	v_cvt_pk_fp8_f32 v6, v12, v13
	ds_read2_b32 v[12:13], v153 offset0:192 offset1:224
	v_cvt_pk_fp8_f32 v4, v8, v9 op_sel:[0,0,1]
	s_waitcnt lgkmcnt(1)
	v_cvt_pk_fp8_f32 v7, v14, v15
	v_cvt_pk_fp8_f32 v5, v10, v11 op_sel:[0,0,1]
	v_cvt_pk_fp8_f32 v6, v0, v1 op_sel:[0,0,1]
	ds_read2_b32 v[0:1], v150 offset1:32
	s_waitcnt lgkmcnt(1)
	v_cvt_pk_fp8_f32 v7, v12, v13 op_sel:[0,0,1]
	v_lshl_add_u64 v[8:9], s[8:9], 0, v[128:129]
	s_add_u32 s8, s14, 0x8000
	s_addc_u32 s9, s15, 0
	global_store_dwordx4 v[8:9], v[4:7], off nt
	ds_read2_b32 v[8:9], v150 offset0:64 offset1:96
	s_nop 0
	s_waitcnt lgkmcnt(1)
	v_cvt_pk_fp8_f32 v4, v0, v1
	ds_read2_b32 v[0:1], v150 offset0:128 offset1:160
	ds_read2_b32 v[10:11], v150 offset0:192 offset1:224
	ds_read2_b32 v[12:13], v154 offset1:32
	s_waitcnt lgkmcnt(2)
	v_cvt_pk_fp8_f32 v5, v0, v1
	ds_read2_b32 v[0:1], v154 offset0:64 offset1:96
	ds_read2_b32 v[14:15], v154 offset0:128 offset1:160
	s_waitcnt lgkmcnt(2)
	v_cvt_pk_fp8_f32 v6, v12, v13
	ds_read2_b32 v[12:13], v154 offset0:192 offset1:224
	v_cvt_pk_fp8_f32 v4, v8, v9 op_sel:[0,0,1]
	s_waitcnt lgkmcnt(1)
	v_cvt_pk_fp8_f32 v7, v14, v15
	v_cvt_pk_fp8_f32 v5, v10, v11 op_sel:[0,0,1]
	v_cvt_pk_fp8_f32 v6, v0, v1 op_sel:[0,0,1]
	ds_read2_b32 v[8:9], v151 offset1:32
	s_waitcnt lgkmcnt(1)
	v_cvt_pk_fp8_f32 v7, v12, v13 op_sel:[0,0,1]
	v_lshl_add_u64 v[0:1], s[8:9], 0, v[128:129]
	s_add_u32 s8, s14, 0xc000
	s_addc_u32 s9, s15, 0
	global_store_dwordx4 v[0:1], v[4:7], off nt
	ds_read2_b32 v[4:5], v151 offset0:64 offset1:96
	s_waitcnt lgkmcnt(1)
	v_cvt_pk_fp8_f32 v0, v8, v9
	ds_read2_b32 v[6:7], v151 offset0:128 offset1:160
	ds_read2_b32 v[8:9], v151 offset0:192 offset1:224
	ds_read2_b32 v[10:11], v155 offset1:32
	s_waitcnt lgkmcnt(3)
	v_cvt_pk_fp8_f32 v0, v4, v5 op_sel:[0,0,1]
	s_waitcnt lgkmcnt(2)
	v_cvt_pk_fp8_f32 v1, v6, v7
	ds_read2_b32 v[6:7], v155 offset0:128 offset1:160
	ds_read2_b32 v[12:13], v155 offset0:64 offset1:96
	s_waitcnt lgkmcnt(2)
	v_cvt_pk_fp8_f32 v2, v10, v11
	ds_read2_b32 v[10:11], v155 offset0:192 offset1:224
	v_cvt_pk_fp8_f32 v1, v8, v9 op_sel:[0,0,1]
	s_waitcnt lgkmcnt(2)
	v_cvt_pk_fp8_f32 v3, v6, v7
	s_waitcnt lgkmcnt(1)
	v_cvt_pk_fp8_f32 v2, v12, v13 op_sel:[0,0,1]
	v_lshl_add_u64 v[4:5], s[8:9], 0, v[128:129]
	s_andn2_b64 vcc, exec, s[20:21]
	s_waitcnt lgkmcnt(0)
	v_cvt_pk_fp8_f32 v3, v10, v11 op_sel:[0,0,1]
	s_mov_b64 s[20:21], -1
	global_store_dwordx4 v[4:5], v[0:3], off nt
	s_waitcnt lgkmcnt(0)
	s_cbranch_vccnz .LBB0_488
	s_add_i32 s1, s0, s1
	s_cmp_lt_i32 s1, s45
	s_cselect_b32 s1, s1, s3
	s_cmp_lt_i32 s1, 0x10000
	s_cselect_b64 s[14:15], -1, 0
	s_cmp_gt_i32 s1, 0xffff
	s_mov_b64 s[24:25], -1
	s_cbranch_scc0 .LBB0_497
	s_add_i32 s8, s1, 0xffff0000
	s_lshr_b32 s12, s8, 10
	s_and_b32 s9, s1, 0x3ff
	s_lshl_b64 s[10:11], s[12:13], 22
	s_lshl_b64 s[20:21], s[12:13], 24
	s_add_u32 s22, s6, s20
	s_addc_u32 s23, s7, s21
	s_add_u32 s20, s77, s10
	v_readlane_b32 s8, v252, 33
	s_addc_u32 s21, s8, s11
	s_mov_b64 s[24:25], 0

; __device__ __forceinline__ void mask_tile(f32x16& p0, f32x16& p1, int dq, unsigned W) {
;     const float NEG = -__builtin_inff();
; #pragma unroll
;     for (int r = 0; r < 16; ++r) {
;         const int c = (r & 3) + 8 * (r >> 2);
;         if ((unsigned)(dq - c) >= W) p0[r] = NEG;
;         if ((unsigned)(dq - c - 32) >= W) p1[r] = NEG;
;     }
; }
; __device__ __forceinline__ void finishSM(f32x16& p0, f32x16& p1, i32x8& pa) {
;     for (int r = 0; r < 16; ++r) p1[r] = __builtin_amdgcn_exp2f(p1[r]);
; #pragma unroll
;     for (int v = 0; v < 4; ++v) { pa[v] = (int)cvt_pk4_fp8(p0[4 * v], p0[4 * v + 1], p0[4 * v + 2], p0[4 * v + 3]); pa[4 + v] = (int)cvt_pk4_fp8(p1[4 * v], p1[4 * v + 1], p1[4 * v + 2], p1[4 * v + 3]); }
; }
; __device__ __forceinline__ void qkt(f32x16& p0, f32x16& p1, const char* stg, int ka, const i32x8* qf, const f32x16& minit) {
;     p0 = minit; p1 = minit;
; #pragma unroll
;     for (int s = 0; s < 3; ++s) { const char* a = stg + SOFF_K + s * 4096 + ka; const char* b = stg + SOFF_K + s * 4096 + (ka ^ 16);
;         const i32x4 a0 = *reinterpret_cast<const i32x4*>(a), a1 = *reinterpret_cast<const i32x4*>(b);
;         const i32x4 c0 = *reinterpret_cast<const i32x4*>(a + 2048), c1 = *reinterpret_cast<const i32x4*>(b + 2048);
;         p0 = __builtin_amdgcn_mfma_scale_f32_32x32x64_f8f6f4(__builtin_shufflevector(a0, a1, 0, 1, 2, 3, 4, 5, 6, 7), qf[s], p0, 0, 0, 0, 0, 0, 0);
;         p1 = __builtin_amdgcn_mfma_scale_f32_32x32x64_f8f6f4(__builtin_shufflevector(c0, c1, 0, 1, 2, 3, 4, 5, 6, 7), qf[s], p1, 0, 0, 0, 0, 0, 0); }
; }
; __device__ __forceinline__ void v_read(i32x8 (&vf)[4], const char* stg, int ka) {
; #pragma unroll
;     for (int d0 = 0; d0 < 4; ++d0) { const i32x4 a0 = *reinterpret_cast<const i32x4*>(stg + SOFF_V + d0 * 2048 + ka), a1 = *reinterpret_cast<const i32x4*>(stg + SOFF_V + d0 * 2048 + (ka ^ 16));
;         vf[d0] = __builtin_shufflevector(a0, a1, 0, 1, 2, 3, 4, 5, 6, 7); }
; }
; __device__ __forceinline__ void pv_mma(f32x16* o, f32x16& ol, const i32x8 (&vf)[4], const i32x8 ones, const i32x8 pa) {
; #pragma unroll
;     for (int d0 = 0; d0 < 4; ++d0) o[d0] = __builtin_amdgcn_mfma_scale_f32_32x32x64_f8f6f4(pa, vf[d0], o[d0], 0, 0, 0, 0, 0, 0);
;     ol = __builtin_amdgcn_mfma_scale_f32_32x32x64_f8f6f4(pa, ones, ol, 0, 0, 0, 0, 0, 0);
; }
.LBB0_532:
	s_cmp_gt_i32 s1, 4
	s_cselect_b32 s46, -5, 1
	s_add_i32 s46, s46, s1
	s_mulk_i32 s46, 0x5000
	s_add_i32 s46, s46, 0
	v_add_u32_e32 v199, s46, v193
	v_add_u32_e32 v200, s46, v194
	ds_read_b128 v[112:115], v199
	ds_read_b128 v[116:119], v200
	ds_read_b128 v[218:221], v199 offset:2048
	ds_read_b128 v[222:225], v200 offset:2048
	ds_read_b128 v[236:239], v199 offset:4096
	ds_read_b128 v[240:243], v200 offset:4096
	ds_read_b128 v[244:247], v199 offset:6144
	ds_read_b128 v[248:251], v200 offset:6144
	v_exp_f32_e32 v217, v96
	s_waitcnt lgkmcnt(6)
	v_mfma_f32_32x32x64_f8f6f4 v[128:143], v[112:119], v[168:175], v[80:95]
	v_exp_f32_e32 v97, v97
	v_exp_f32_e32 v98, v98
	v_exp_f32_e32 v99, v99
	v_exp_f32_e32 v102, v102
	v_exp_f32_e32 v104, v104
	v_exp_f32_e32 v105, v105
	v_exp_f32_e32 v108, v108
	v_exp_f32_e32 v109, v109
	v_exp_f32_e32 v106, v106
	v_exp_f32_e32 v107, v107
	v_exp_f32_e32 v110, v110
	v_exp_f32_e32 v111, v111
	s_waitcnt lgkmcnt(4)
	v_mfma_f32_32x32x64_f8f6f4 v[112:127], v[218:225], v[168:175], v[80:95]
	ds_read_b128 v[218:221], v199 offset:8192
	ds_read_b128 v[222:225], v200 offset:8192
	ds_read_b128 v[226:229], v199 offset:10240
	ds_read_b128 v[230:233], v200 offset:10240
	s_waitcnt lgkmcnt(6)
	v_mfma_f32_32x32x64_f8f6f4 v[128:143], v[236:243], v[176:183], v[128:143]
	s_waitcnt lgkmcnt(4)
	v_mfma_f32_32x32x64_f8f6f4 v[112:127], v[244:251], v[176:183], v[112:127]
	s_mul_i32 s98, s1, 0x5000
	v_add_u32_e32 v253, s98, v193
	v_add_u32_e32 v254, s98, v194
	ds_read_b128 v[240:243], v254 offset:12288
	ds_read_b128 v[236:239], v253 offset:12288
	ds_read_b128 v[244:247], v253 offset:14336
	ds_read_b128 v[248:251], v254 offset:14336
	s_waitcnt lgkmcnt(6)
	v_mfma_f32_32x32x64_f8f6f4 v[128:143], v[218:225], v[160:167], v[128:143]
	v_exp_f32_e32 v218, v100
	v_exp_f32_e32 v219, v101
	v_exp_f32_e32 v220, v103
	s_nop 0
	v_cvt_pk_fp8_f32 v100, v217, v97
	v_cvt_pk_fp8_f32 v101, v218, v219
	v_cvt_pk_fp8_f32 v100, v98, v99 op_sel:[0,0,1]
	v_cvt_pk_fp8_f32 v101, v102, v220 op_sel:[0,0,1]
	s_waitcnt lgkmcnt(4)
	v_mfma_f32_32x32x64_f8f6f4 v[112:127], v[226:233], v[160:167], v[112:127]
	v_cvt_pk_fp8_f32 v96, v215, v216
	v_cvt_pk_fp8_f32 v97, v211, v212
	v_cvt_pk_fp8_f32 v98, v207, v208
	v_cvt_pk_fp8_f32 v102, v104, v105
	v_cvt_pk_fp8_f32 v99, v203, v204
	v_cvt_pk_fp8_f32 v103, v108, v109
	v_cvt_pk_fp8_f32 v96, v213, v214 op_sel:[0,0,1]
	v_cvt_pk_fp8_f32 v97, v209, v210 op_sel:[0,0,1]
	v_cvt_pk_fp8_f32 v98, v205, v206 op_sel:[0,0,1]
	v_cvt_pk_fp8_f32 v102, v106, v107 op_sel:[0,0,1]
	v_cvt_pk_fp8_f32 v99, v201, v202 op_sel:[0,0,1]
	v_cvt_pk_fp8_f32 v103, v110, v111 op_sel:[0,0,1]
	s_mul_i32 s46, s1, 0x5000
	s_add_i32 s46, s46, 0
	v_add_u32_e32 v202, s46, v194
	v_add_u32_e32 v201, s46, v193
	ds_read_b128 v[108:111], v202 offset:16384
	ds_read_b128 v[104:107], v201 offset:16384
	v_mfma_f32_32x32x64_f8f6f4 v[64:79], v[96:103], v[152:159], v[64:79]
	s_sub_i32 s46, s38, 64
	s_cmp_le_i32 s46, s0
	s_waitcnt lgkmcnt(4)
	v_mfma_f32_32x32x64_f8f6f4 v[48:63], v[96:103], v[236:243], v[48:63]
	ds_read_b128 v[236:239], v201 offset:18432
	ds_read_b128 v[240:243], v202 offset:18432
	s_waitcnt lgkmcnt(4)
	v_mfma_f32_32x32x64_f8f6f4 v[32:47], v[96:103], v[244:251], v[32:47]
	s_waitcnt lgkmcnt(2)
	v_mfma_f32_32x32x64_f8f6f4 v[16:31], v[96:103], v[104:111], v[16:31]
	s_waitcnt lgkmcnt(0)
	v_mfma_f32_32x32x64_f8f6f4 v[0:15], v[96:103], v[236:243], v[0:15]
	s_cbranch_scc1 .LBB0_534
	v_add_u32_e32 v96, 0x4000007b, v196
	v_cmp_gt_u32_e32 vcc, 2.0, v96
	v_add_u32_e32 v96, 0x5b, v196
	s_nop 0
	v_cndmask_b32_e32 v128, v187, v128, vcc
	v_cmp_lt_u32_e32 vcc, s3, v96
	v_add_u32_e32 v96, 0x7a, v196
	s_nop 0
	v_cndmask_b32_e32 v112, v187, v112, vcc
	v_cmp_lt_u32_e32 vcc, s3, v96
	v_add_u32_e32 v96, 0x5a, v196
	s_nop 0
	v_cndmask_b32_e32 v129, v187, v129, vcc
	v_cmp_lt_u32_e32 vcc, s3, v96
	v_add_u32_e32 v96, 0x79, v196
	s_nop 0
	v_cndmask_b32_e32 v113, v187, v113, vcc
	v_cmp_lt_u32_e32 vcc, s3, v96
	v_add_u32_e32 v96, 0x59, v196
	s_nop 0
	v_cndmask_b32_e32 v130, v187, v130, vcc
	v_cmp_lt_u32_e32 vcc, s3, v96
	v_add_u32_e32 v96, 0x78, v196
	s_nop 0
	v_cndmask_b32_e32 v114, v187, v114, vcc
	v_cmp_lt_u32_e32 vcc, s3, v96
	v_add_u32_e32 v96, 0x58, v196
	s_nop 0
	v_cndmask_b32_e32 v131, v187, v131, vcc
	v_cmp_lt_u32_e32 vcc, s3, v96
	v_add_u32_e32 v96, 0x73, v196
	s_nop 0
	v_cndmask_b32_e32 v115, v187, v115, vcc
	v_cmp_lt_u32_e32 vcc, s3, v96
	v_add_u32_e32 v96, 0x53, v196
	s_nop 0
	v_cndmask_b32_e32 v132, v187, v132, vcc
	v_cmp_lt_u32_e32 vcc, s3, v96
	v_add_u32_e32 v96, 0x72, v196
	s_nop 0
	v_cndmask_b32_e32 v116, v187, v116, vcc
	v_cmp_lt_u32_e32 vcc, s3, v96
	v_add_u32_e32 v96, 0x52, v196
	s_nop 0
	v_cndmask_b32_e32 v133, v187, v133, vcc
	v_cmp_lt_u32_e32 vcc, s3, v96
	v_add_u32_e32 v96, 0x71, v196
	s_nop 0
	v_cndmask_b32_e32 v117, v187, v117, vcc
	v_cmp_lt_u32_e32 vcc, s3, v96
	v_add_u32_e32 v96, 0x51, v196
	s_nop 0
	v_cndmask_b32_e32 v134, v187, v134, vcc
	v_cmp_lt_u32_e32 vcc, s3, v96
	v_add_u32_e32 v96, 0x70, v196
	s_nop 0
	v_cndmask_b32_e32 v118, v187, v118, vcc
	v_cmp_lt_u32_e32 vcc, s3, v96
	v_add_u32_e32 v96, 0x50, v196
	s_nop 0
	v_cndmask_b32_e32 v135, v187, v135, vcc
	v_cmp_lt_u32_e32 vcc, s3, v96
	v_add_u32_e32 v96, 0x6b, v196
	s_nop 0
	v_cndmask_b32_e32 v119, v187, v119, vcc
	v_cmp_lt_u32_e32 vcc, s3, v96
	v_add_u32_e32 v96, 0x4b, v196
	s_nop 0
	v_cndmask_b32_e32 v136, v187, v136, vcc
	v_cmp_lt_u32_e32 vcc, s3, v96
	v_add_u32_e32 v96, 0x6a, v196
	s_nop 0
	v_cndmask_b32_e32 v120, v187, v120, vcc
	v_cmp_lt_u32_e32 vcc, s3, v96
	v_add_u32_e32 v96, 0x4a, v196
	s_nop 0
	v_cndmask_b32_e32 v137, v187, v137, vcc
	v_cmp_lt_u32_e32 vcc, s3, v96
	v_add_u32_e32 v96, 0x69, v196
	s_nop 0
	v_cndmask_b32_e32 v121, v187, v121, vcc
	v_cmp_lt_u32_e32 vcc, s3, v96
	v_add_u32_e32 v96, 0x49, v196
	s_nop 0
	v_cndmask_b32_e32 v138, v187, v138, vcc
	v_cmp_lt_u32_e32 vcc, s3, v96
	v_add_u32_e32 v96, 0x68, v196
	s_nop 0
	v_cndmask_b32_e32 v122, v187, v122, vcc
	v_cmp_lt_u32_e32 vcc, s3, v96
	v_add_u32_e32 v96, 0x48, v196
	s_nop 0
	v_cndmask_b32_e32 v139, v187, v139, vcc
	v_cmp_lt_u32_e32 vcc, s3, v96
	v_add_u32_e32 v96, 0x63, v196
	s_nop 0
	v_cndmask_b32_e32 v123, v187, v123, vcc
	v_cmp_lt_u32_e32 vcc, s3, v96
	v_add_u32_e32 v96, 0x43, v196
	s_nop 0
	v_cndmask_b32_e32 v140, v187, v140, vcc
	v_cmp_lt_u32_e32 vcc, s3, v96
	v_add_u32_e32 v96, 0x62, v196
	s_nop 0
	v_cndmask_b32_e32 v124, v187, v124, vcc
	v_cmp_lt_u32_e32 vcc, s3, v96
	v_add_u32_e32 v96, 0x42, v196
	s_nop 0
	v_cndmask_b32_e32 v141, v187, v141, vcc
	v_cmp_lt_u32_e32 vcc, s3, v96
	v_add_u32_e32 v96, 0x61, v196
	s_nop 0
	v_cndmask_b32_e32 v125, v187, v125, vcc
	v_cmp_lt_u32_e32 vcc, s3, v96
	v_add_u32_e32 v96, 0x41, v196
	s_nop 0
	v_cndmask_b32_e32 v142, v187, v142, vcc
	v_cmp_lt_u32_e32 vcc, s3, v96
	v_add_u32_e32 v96, 0x60, v196
	s_nop 0
	v_cndmask_b32_e32 v126, v187, v126, vcc
	v_cmp_lt_u32_e32 vcc, s3, v96
	v_add_u32_e32 v96, 64, v196
	s_nop 0
	v_cndmask_b32_e32 v143, v187, v143, vcc
	v_cmp_lt_u32_e32 vcc, s3, v96
	s_nop 1
	v_cndmask_b32_e32 v127, v187, v127, vcc

; __device__ __forceinline__ unsigned cvt_pk4_fp8(float a, float b, float c, float d) { int w; asm("" : "=v"(w));     w = __builtin_amdgcn_cvt_pk_fp8_f32(a, b, w, false); w = __builtin_amdgcn_cvt_pk_fp8_f32(c, d, w, true); return (unsigned)w; }
; __device__ __forceinline__ void finishSM(f32x16& p0, f32x16& p1, i32x8& pa) {
;     for (int r = 0; r < 16; ++r) p1[r] = __builtin_amdgcn_exp2f(p1[r]);
; #pragma unroll
;     for (int v = 0; v < 4; ++v) { pa[v] = (int)cvt_pk4_fp8(p0[4 * v], p0[4 * v + 1], p0[4 * v + 2], p0[4 * v + 3]); pa[4 + v] = (int)cvt_pk4_fp8(p1[4 * v], p1[4 * v + 1], p1[4 * v + 2], p1[4 * v + 3]); }
; }
; __device__ __forceinline__ void qkt(f32x16& p0, f32x16& p1, const char* stg, int ka, const i32x8* qf, const f32x16& minit) {
;     p0 = minit; p1 = minit;
; #pragma unroll
;     for (int s = 0; s < 3; ++s) { const char* a = stg + SOFF_K + s * 4096 + ka; const char* b = stg + SOFF_K + s * 4096 + (ka ^ 16);
;         const i32x4 a0 = *reinterpret_cast<const i32x4*>(a), a1 = *reinterpret_cast<const i32x4*>(b);
;         const i32x4 c0 = *reinterpret_cast<const i32x4*>(a + 2048), c1 = *reinterpret_cast<const i32x4*>(b + 2048);
;         p0 = __builtin_amdgcn_mfma_scale_f32_32x32x64_f8f6f4(__builtin_shufflevector(a0, a1, 0, 1, 2, 3, 4, 5, 6, 7), qf[s], p0, 0, 0, 0, 0, 0, 0);
;         p1 = __builtin_amdgcn_mfma_scale_f32_32x32x64_f8f6f4(__builtin_shufflevector(c0, c1, 0, 1, 2, 3, 4, 5, 6, 7), qf[s], p1, 0, 0, 0, 0, 0, 0); }
; }
; __device__ __forceinline__ void v_read(i32x8 (&vf)[4], const char* stg, int ka) {
; #pragma unroll
;     for (int d0 = 0; d0 < 4; ++d0) { const i32x4 a0 = *reinterpret_cast<const i32x4*>(stg + SOFF_V + d0 * 2048 + ka), a1 = *reinterpret_cast<const i32x4*>(stg + SOFF_V + d0 * 2048 + (ka ^ 16));
;         vf[d0] = __builtin_shufflevector(a0, a1, 0, 1, 2, 3, 4, 5, 6, 7); }
; }
; __device__ __forceinline__ void pv_mma(f32x16* o, f32x16& ol, const i32x8 (&vf)[4], const i32x8 ones, const i32x8 pa) {
; #pragma unroll
;     for (int d0 = 0; d0 < 4; ++d0) o[d0] = __builtin_amdgcn_mfma_scale_f32_32x32x64_f8f6f4(pa, vf[d0], o[d0], 0, 0, 0, 0, 0, 0);
;     ol = __builtin_amdgcn_mfma_scale_f32_32x32x64_f8f6f4(pa, ones, ol, 0, 0, 0, 0, 0, 0);
; }
.LBB0_539:
	s_cmp_gt_i32 s1, 3
	s_cselect_b32 s46, -4, 2
	s_add_i32 s1, s46, s1
	v_exp_f32_e32 v201, v128
	v_exp_f32_e32 v218, v129
	v_exp_f32_e32 v219, v130
	v_exp_f32_e32 v220, v131
	v_exp_f32_e32 v221, v132
	v_exp_f32_e32 v222, v133
	v_exp_f32_e32 v223, v134
	v_exp_f32_e32 v224, v135
	v_exp_f32_e32 v225, v136
	v_exp_f32_e32 v226, v137
	v_exp_f32_e32 v227, v138
	v_exp_f32_e32 v228, v139
	v_exp_f32_e32 v229, v140
	v_exp_f32_e32 v230, v141
	v_exp_f32_e32 v231, v142
	v_exp_f32_e32 v232, v143
	s_mul_i32 s92, s1, 0x5000
	s_add_i32 s46, s92, 0
	v_add_u32_e32 v233, s46, v193
	v_add_u32_e32 v234, s46, v194
	ds_read_b128 v[202:205], v233
	ds_read_b128 v[206:209], v234
	ds_read_b128 v[210:213], v233 offset:2048
	ds_read_b128 v[214:217], v234 offset:2048
	ds_read_b128 v[236:239], v233 offset:4096
	ds_read_b128 v[240:243], v234 offset:4096
	ds_read_b128 v[244:247], v233 offset:6144
	ds_read_b128 v[248:251], v234 offset:6144
	v_exp_f32_e32 v113, v113
	s_waitcnt lgkmcnt(6)
	v_mfma_f32_32x32x64_f8f6f4 v[128:143], v[202:209], v[168:175], v[96:111]
	v_exp_f32_e32 v114, v114
	v_exp_f32_e32 v115, v115
	v_exp_f32_e32 v118, v118
	v_exp_f32_e32 v120, v120
	v_exp_f32_e32 v121, v121
	v_exp_f32_e32 v124, v124
	v_exp_f32_e32 v125, v125
	v_exp_f32_e32 v122, v122
	v_exp_f32_e32 v123, v123
	v_exp_f32_e32 v126, v126
	v_exp_f32_e32 v127, v127
	s_waitcnt lgkmcnt(4)
	v_mfma_f32_32x32x64_f8f6f4 v[96:111], v[210:217], v[168:175], v[96:111]
	ds_read_b128 v[202:205], v233 offset:8192
	ds_read_b128 v[206:209], v234 offset:8192
	ds_read_b128 v[210:213], v233 offset:10240
	ds_read_b128 v[214:217], v234 offset:10240
	s_waitcnt lgkmcnt(6)
	v_mfma_f32_32x32x64_f8f6f4 v[128:143], v[236:243], v[176:183], v[128:143]
	s_waitcnt lgkmcnt(4)
	v_mfma_f32_32x32x64_f8f6f4 v[96:111], v[244:251], v[176:183], v[96:111]
	ds_read_b128 v[240:243], v200 offset:12288
	ds_read_b128 v[236:239], v199 offset:12288
	ds_read_b128 v[244:247], v199 offset:14336
	ds_read_b128 v[248:251], v200 offset:14336
	s_waitcnt lgkmcnt(6)
	v_mfma_f32_32x32x64_f8f6f4 v[128:143], v[202:209], v[160:167], v[128:143]
	v_exp_f32_e32 v202, v112
	v_exp_f32_e32 v203, v116
	v_exp_f32_e32 v204, v117
	v_exp_f32_e32 v205, v119
	s_nop 0
	v_cvt_pk_fp8_f32 v116, v202, v113
	v_cvt_pk_fp8_f32 v117, v203, v204
	v_cvt_pk_fp8_f32 v116, v114, v115 op_sel:[0,0,1]
	v_cvt_pk_fp8_f32 v117, v118, v205 op_sel:[0,0,1]
	s_waitcnt lgkmcnt(4)
	v_mfma_f32_32x32x64_f8f6f4 v[96:111], v[210:217], v[160:167], v[96:111]
	v_cvt_pk_fp8_f32 v112, v201, v218
	v_cvt_pk_fp8_f32 v113, v221, v222
	v_cvt_pk_fp8_f32 v114, v225, v226
	v_cvt_pk_fp8_f32 v118, v120, v121
	v_cvt_pk_fp8_f32 v115, v229, v230
	v_cvt_pk_fp8_f32 v119, v124, v125
	v_cvt_pk_fp8_f32 v112, v219, v220 op_sel:[0,0,1]
	v_cvt_pk_fp8_f32 v113, v223, v224 op_sel:[0,0,1]
	v_cvt_pk_fp8_f32 v114, v227, v228 op_sel:[0,0,1]
	v_cvt_pk_fp8_f32 v118, v122, v123 op_sel:[0,0,1]
	v_cvt_pk_fp8_f32 v115, v231, v232 op_sel:[0,0,1]
	v_cvt_pk_fp8_f32 v119, v126, v127 op_sel:[0,0,1]
	ds_read_b128 v[124:127], v200 offset:16384
	ds_read_b128 v[120:123], v199 offset:16384
	v_mfma_f32_32x32x64_f8f6f4 v[64:79], v[112:119], v[152:159], v[64:79]
	s_cmp_le_i32 s38, s0
	s_waitcnt lgkmcnt(4)
	v_mfma_f32_32x32x64_f8f6f4 v[48:63], v[112:119], v[236:243], v[48:63]
	ds_read_b128 v[236:239], v199 offset:18432
	ds_read_b128 v[240:243], v200 offset:18432
	s_waitcnt lgkmcnt(4)
	v_mfma_f32_32x32x64_f8f6f4 v[32:47], v[112:119], v[244:251], v[32:47]
	s_waitcnt lgkmcnt(2)
	v_mfma_f32_32x32x64_f8f6f4 v[16:31], v[112:119], v[120:127], v[16:31]
	s_waitcnt lgkmcnt(0)
	v_mfma_f32_32x32x64_f8f6f4 v[0:15], v[112:119], v[236:243], v[0:15]
	s_cbranch_scc1 .LBB0_541
; __device__ __forceinline__ void mask_tile(f32x16& p0, f32x16& p1, int dq, unsigned W) {
;     const float NEG = -__builtin_inff();
; #pragma unroll
;     for (int r = 0; r < 16; ++r) {
;         const int c = (r & 3) + 8 * (r >> 2);
;         if ((unsigned)(dq - c) >= W) p0[r] = NEG;
;         if ((unsigned)(dq - c - 32) >= W) p1[r] = NEG;
;     }
; }
	v_add_u32_e32 v112, 0x4000003b, v196
	v_cmp_gt_u32_e32 vcc, 2.0, v112
	v_add_u32_e32 v112, 27, v196
	s_nop 0
	v_cndmask_b32_e32 v128, v187, v128, vcc
	v_cmp_lt_u32_e32 vcc, s3, v112
	v_add_u32_e32 v112, 58, v196
	s_nop 0
	v_cndmask_b32_e32 v96, v187, v96, vcc
	v_cmp_lt_u32_e32 vcc, s3, v112
	v_add_u32_e32 v112, 26, v196
	s_nop 0
	v_cndmask_b32_e32 v129, v187, v129, vcc
	v_cmp_lt_u32_e32 vcc, s3, v112
	v_add_u32_e32 v112, 57, v196
	s_nop 0
	v_cndmask_b32_e32 v97, v187, v97, vcc
	v_cmp_lt_u32_e32 vcc, s3, v112
	v_add_u32_e32 v112, 25, v196
	s_nop 0
	v_cndmask_b32_e32 v130, v187, v130, vcc
	v_cmp_lt_u32_e32 vcc, s3, v112
	v_add_u32_e32 v112, 56, v196
	s_nop 0
	v_cndmask_b32_e32 v98, v187, v98, vcc
	v_cmp_lt_u32_e32 vcc, s3, v112
	v_add_u32_e32 v112, 24, v196
	s_nop 0
	v_cndmask_b32_e32 v131, v187, v131, vcc
	v_cmp_lt_u32_e32 vcc, s3, v112
	v_add_u32_e32 v112, 51, v196
	s_nop 0
	v_cndmask_b32_e32 v99, v187, v99, vcc
	v_cmp_lt_u32_e32 vcc, s3, v112
	v_add_u32_e32 v112, 19, v196
	s_nop 0
	v_cndmask_b32_e32 v132, v187, v132, vcc
	v_cmp_lt_u32_e32 vcc, s3, v112
	v_add_u32_e32 v112, 50, v196
	s_nop 0
	v_cndmask_b32_e32 v100, v187, v100, vcc
	v_cmp_lt_u32_e32 vcc, s3, v112
	v_add_u32_e32 v112, 18, v196
	s_nop 0
	v_cndmask_b32_e32 v133, v187, v133, vcc
	v_cmp_lt_u32_e32 vcc, s3, v112
	v_add_u32_e32 v112, 49, v196
	s_nop 0
	v_cndmask_b32_e32 v101, v187, v101, vcc
	v_cmp_lt_u32_e32 vcc, s3, v112
	v_add_u32_e32 v112, 17, v196
	s_nop 0
	v_cndmask_b32_e32 v134, v187, v134, vcc
	v_cmp_lt_u32_e32 vcc, s3, v112
	v_add_u32_e32 v112, 48, v196
	s_nop 0
	v_cndmask_b32_e32 v102, v187, v102, vcc
	v_cmp_lt_u32_e32 vcc, s3, v112
	v_add_u32_e32 v112, 16, v196
	s_nop 0
	v_cndmask_b32_e32 v135, v187, v135, vcc
	v_cmp_lt_u32_e32 vcc, s3, v112
	v_add_u32_e32 v112, 43, v196
	s_nop 0
	v_cndmask_b32_e32 v103, v187, v103, vcc
	v_cmp_lt_u32_e32 vcc, s3, v112
	v_add_u32_e32 v112, 11, v196
	s_nop 0
	v_cndmask_b32_e32 v136, v187, v136, vcc
	v_cmp_lt_u32_e32 vcc, s3, v112
	v_add_u32_e32 v112, 42, v196
	s_nop 0
	v_cndmask_b32_e32 v104, v187, v104, vcc
	v_cmp_lt_u32_e32 vcc, s3, v112
	v_add_u32_e32 v112, 10, v196
	s_nop 0
	v_cndmask_b32_e32 v137, v187, v137, vcc
	v_cmp_lt_u32_e32 vcc, s3, v112
	v_add_u32_e32 v112, 41, v196
	s_nop 0
	v_cndmask_b32_e32 v105, v187, v105, vcc
	v_cmp_lt_u32_e32 vcc, s3, v112
	v_add_u32_e32 v112, 9, v196
	s_nop 0
	v_cndmask_b32_e32 v138, v187, v138, vcc
	v_cmp_lt_u32_e32 vcc, s3, v112
	v_add_u32_e32 v112, 40, v196
	s_nop 0
	v_cndmask_b32_e32 v106, v187, v106, vcc
	v_cmp_lt_u32_e32 vcc, s3, v112
	v_add_u32_e32 v112, 8, v196
	s_nop 0
	v_cndmask_b32_e32 v139, v187, v139, vcc
	v_cmp_lt_u32_e32 vcc, s3, v112
	v_add_u32_e32 v112, 35, v196
	s_nop 0
	v_cndmask_b32_e32 v107, v187, v107, vcc
	v_cmp_lt_u32_e32 vcc, s3, v112
	v_add_u32_e32 v112, 3, v196
	s_nop 0
	v_cndmask_b32_e32 v140, v187, v140, vcc
	v_cmp_lt_u32_e32 vcc, s3, v112
	v_add_u32_e32 v112, 34, v196
	s_nop 0
	v_cndmask_b32_e32 v108, v187, v108, vcc
	v_cmp_lt_u32_e32 vcc, s3, v112
	v_add_u32_e32 v112, 2, v196
	s_nop 0
	v_cndmask_b32_e32 v141, v187, v141, vcc
	v_cmp_lt_u32_e32 vcc, s3, v112
	v_add_u32_e32 v112, 33, v196
	s_nop 0
	v_cndmask_b32_e32 v109, v187, v109, vcc
	v_cmp_lt_u32_e32 vcc, s3, v112
	v_add_u32_e32 v112, 1, v196
	s_nop 0
	v_cndmask_b32_e32 v142, v187, v142, vcc
	v_cmp_lt_u32_e32 vcc, s3, v112
	v_add_u32_e32 v112, 32, v196
	s_nop 0
	v_cndmask_b32_e32 v110, v187, v110, vcc
	v_cmp_lt_u32_e32 vcc, s3, v112
	s_nop 1
	v_cndmask_b32_e32 v143, v187, v143, vcc
	v_cmp_lt_u32_e32 vcc, s3, v196
	s_nop 1
	v_cndmask_b32_e32 v111, v187, v111, vcc

; __device__ __forceinline__ cgptr cuni(const void* p) { const unsigned long long v = (unsigned long long)p; const unsigned lo = __builtin_amdgcn_readfirstlane((unsigned)v), hi = __builtin_amdgcn_readfirstlane((unsigned)(v >> 32)); return (cgptr)(((unsigned long long)hi << 32) | lo); }
; #define CONV_LOAD(v, c) do { const unsigned lo_ = (unsigned)(lane >> 3) * (c).N4 + 16u * (unsigned)(lane & 7); _Pragma("unroll") for (int i = 0; i < 16; ++i) v[i] = __builtin_nontemporal_load((const GAS f32x4*)(cuni((const void*)((c).src + (size_t)(8 * i) * (c).N4)) + lo_)); } while (0)
; __device__ __forceinline__ ConvItem conv_decode(int it, const float* wgu, const float* wd, unsigned char* WguT, unsigned char* WdT) {
;     constexpr int I_GU = NE * 16 * 128;
;     ConvItem c; int r = it, nbn, N; const float* src; unsigned char* dstp; bool gu;
;     if (r < I_GU) { const int e = r / (16 * 128); r -= e * (16 * 128); N = 4096; nbn = 128; src = wgu + (size_t)e * DM * 4096; dstp = WguT + (size_t)e * 4096 * DM; gu = true; }
;     else { r -= I_GU; const int e = r / (16 * 64); r -= e * (16 * 64); N = DM; nbn = 64; src = wd + (size_t)e * DFF * DM; dstp = WdT + (size_t)e * DM * DFF; gu = false; }
;     const int kb = r / nbn, nb = r - kb * nbn, n0 = nb * 32, k0 = kb * 128; int dst = n0;
;     if (gu) { const int j = n0 & 2047; dst = (j >> 7) * 256 + (j & 127) + ((n0 >= 2048) ? 128 : 0); }
;     c.src = cuni(src + (size_t)k0 * N + n0); c.dstp = cuni(dstp + (size_t)dst * DM + k0); c.N4 = (unsigned)N * 4u;
;     return c;
; }
; __device__ __forceinline__ void convert_expert_weights(const float* wgu, const float* wd, unsigned char* WguT, unsigned char* WdT, LAS float* scr, int gw, int NGW, int NIT, int lane) {
;     ...
;         const bool ha = it + NGW < NIT; ca = conv_decode(ha ? it + NGW : it, wgu, wd, WguT, WdT); CONV_LOAD(va, ca);
;         CONV_STORE(vb, cb);
.LBB0_564:
	v_cvt_f32_ubyte0_e32 v64, s12
	v_rcp_iflag_f32_e32 v64, v64
	s_sub_i32 s27, 0, s12
	s_abs_i32 s26, s9
	s_ashr_i32 s17, s9, 31
	v_mul_f32_e32 v64, 0x4f7ffffe, v64
	v_cvt_u32_f32_e32 v64, v64
	v_add_u32_e32 v152, 0x400, v148
	v_add_u32_e32 v153, 0x400, v149
	v_add_u32_e32 v154, 0x400, v150
	v_readfirstlane_b32 s30, v64
	s_mul_i32 s27, s27, s30
	s_mul_hi_u32 s27, s30, s27
	s_add_i32 s30, s30, s27
	s_mul_hi_u32 s27, s26, s30
	s_mul_i32 s30, s27, s12
	s_sub_i32 s26, s26, s30
	s_add_i32 s31, s27, 1
	s_sub_i32 s30, s26, s12
	s_cmp_ge_u32 s26, s12
	s_cselect_b32 s27, s31, s27
	s_cselect_b32 s26, s30, s26
	s_add_i32 s30, s27, 1
	s_cmp_ge_u32 s26, s12
	s_cselect_b32 s26, s30, s27
	s_xor_b32 s26, s26, s17
	s_sub_i32 s17, s26, s17
	s_mul_i32 s12, s17, s12
	s_lshl_b32 s27, s9, 6
	s_sub_i32 s9, s9, s12
	s_lshl_b32 s26, s9, 5
	s_and_b32 s12, s27, 0xf00
	s_and_b32 s27, s26, 0x60
	s_or_b32 s12, s27, s12
	s_cmp_gt_i32 s9, 63
	s_cselect_b32 s9, 0x80, 0
	s_or_b32 s9, s12, s9
	s_and_b64 s[18:19], s[18:19], exec
	s_cselect_b32 s18, s9, s26
	s_lshl_b32 s9, s17, 7
	s_mul_hi_i32 s31, s9, s8
	s_mul_i32 s30, s9, s8
	s_ashr_i32 s12, s9, 31
	s_lshl_b64 s[30:31], s[30:31], 2
	s_add_u32 s17, s24, s30
	s_addc_u32 s19, s25, s31
	s_ashr_i32 s27, s26, 31
	s_lshl_b64 s[24:25], s[26:27], 2
	s_add_u32 s24, s17, s24
	s_addc_u32 s25, s19, s25
	s_ashr_i32 s19, s18, 31
	s_lshl_b64 s[18:19], s[18:19], 11
	s_add_u32 s17, s22, s18
	s_addc_u32 s19, s23, s19
	s_add_u32 s18, s17, s9
	s_addc_u32 s19, s19, s12
	s_lshl_b32 s9, s8, 5
	v_mul_lo_u32 v64, v130, s8
	s_add_u32 s22, s24, s9
	v_or_b32_e32 v64, v64, v131
	s_addc_u32 s23, s25, 0
	s_lshl_b32 s9, s8, 6
	global_load_dwordx4 v[124:127], v64, s[24:25] nt
	global_load_dwordx4 v[116:119], v64, s[22:23] nt
	s_add_u32 s22, s24, s9
	s_addc_u32 s23, s25, 0
	s_mul_i32 s9, s8, 0x60
	s_add_u32 s26, s24, s9
	s_addc_u32 s27, s25, 0
	s_lshl_b32 s9, s8, 7
	global_load_dwordx4 v[120:123], v64, s[22:23] nt
	global_load_dwordx4 v[108:111], v64, s[26:27] nt
	s_add_u32 s22, s24, s9
	s_addc_u32 s23, s25, 0
	s_mul_i32 s9, s8, 0xa0
	s_add_u32 s26, s24, s9
	s_addc_u32 s27, s25, 0
	s_mul_i32 s9, s8, 0xc0
	global_load_dwordx4 v[112:115], v64, s[22:23] nt
	global_load_dwordx4 v[100:103], v64, s[26:27] nt
	s_add_u32 s22, s24, s9
	s_addc_u32 s23, s25, 0
	s_mul_i32 s9, s8, 0xe0
	s_add_u32 s26, s24, s9
	s_addc_u32 s27, s25, 0
	s_lshl_b32 s9, s8, 8
	global_load_dwordx4 v[104:107], v64, s[22:23] nt
	global_load_dwordx4 v[92:95], v64, s[26:27] nt
	s_add_u32 s22, s24, s9
	s_addc_u32 s23, s25, 0
	s_mul_i32 s9, s8, 0x120
	s_add_u32 s26, s24, s9
	s_addc_u32 s27, s25, 0
	s_mul_i32 s9, s8, 0x140
	global_load_dwordx4 v[96:99], v64, s[22:23] nt
	global_load_dwordx4 v[84:87], v64, s[26:27] nt
	s_add_u32 s22, s24, s9
	s_addc_u32 s23, s25, 0
	s_mul_i32 s9, s8, 0x160
	s_add_u32 s26, s24, s9
	s_addc_u32 s27, s25, 0
	s_mul_i32 s9, s8, 0x180
	global_load_dwordx4 v[88:91], v64, s[22:23] nt
	global_load_dwordx4 v[76:79], v64, s[26:27] nt
	s_add_u32 s22, s24, s9
	s_addc_u32 s23, s25, 0
	s_mul_i32 s9, s8, 0x1a0
	s_add_u32 s26, s24, s9
	s_addc_u32 s27, s25, 0
	s_mul_i32 s9, s8, 0x1c0
	global_load_dwordx4 v[80:83], v64, s[22:23] nt
	global_load_dwordx4 v[68:71], v64, s[26:27] nt
	s_add_u32 s22, s24, s9
	s_addc_u32 s23, s25, 0
	s_mulk_i32 s8, 0x1e0
	s_add_u32 s8, s24, s8
	s_waitcnt vmcnt(29)
	v_pk_mul_f32 v[6:7], v[6:7], s[16:17] op_sel_hi:[1,0]
	v_pk_mul_f32 v[4:5], v[4:5], s[16:17] op_sel_hi:[1,0]
	s_waitcnt vmcnt(28)
	v_pk_mul_f32 v[2:3], v[2:3], s[16:17] op_sel_hi:[1,0]
	v_pk_mul_f32 v[0:1], v[0:1], s[16:17] op_sel_hi:[1,0]
	s_addc_u32 s9, s25, 0
	global_load_dwordx4 v[72:75], v64, s[22:23] nt
	s_nop 0
	global_load_dwordx4 v[64:67], v64, s[8:9] nt
	ds_write_b128 v132, v[4:7]
	ds_write_b128 v133, v[0:3]
	s_waitcnt vmcnt(29)
	v_pk_mul_f32 v[2:3], v[14:15], s[16:17] op_sel_hi:[1,0]
	v_pk_mul_f32 v[0:1], v[12:13], s[16:17] op_sel_hi:[1,0]
	ds_write_b128 v134, v[0:3]
	s_waitcnt vmcnt(28)
	v_pk_mul_f32 v[2:3], v[10:11], s[16:17] op_sel_hi:[1,0]
	v_pk_mul_f32 v[0:1], v[8:9], s[16:17] op_sel_hi:[1,0]
	ds_write_b128 v135, v[0:3]
	s_waitcnt vmcnt(27)
	v_pk_mul_f32 v[2:3], v[22:23], s[16:17] op_sel_hi:[1,0]
	v_pk_mul_f32 v[0:1], v[20:21], s[16:17] op_sel_hi:[1,0]
	ds_write_b128 v136, v[0:3]
	s_waitcnt vmcnt(26)
	v_pk_mul_f32 v[2:3], v[18:19], s[16:17] op_sel_hi:[1,0]
	v_pk_mul_f32 v[0:1], v[16:17], s[16:17] op_sel_hi:[1,0]
	ds_write_b128 v137, v[0:3]
	s_waitcnt vmcnt(25)
	v_pk_mul_f32 v[2:3], v[30:31], s[16:17] op_sel_hi:[1,0]
	v_pk_mul_f32 v[0:1], v[28:29], s[16:17] op_sel_hi:[1,0]
	ds_write_b128 v138, v[0:3]
	s_waitcnt vmcnt(24)
	v_pk_mul_f32 v[2:3], v[26:27], s[16:17] op_sel_hi:[1,0]
	v_pk_mul_f32 v[0:1], v[24:25], s[16:17] op_sel_hi:[1,0]
	ds_write_b128 v139, v[0:3]
	s_waitcnt vmcnt(23)
	v_pk_mul_f32 v[2:3], v[38:39], s[16:17] op_sel_hi:[1,0]
	v_pk_mul_f32 v[0:1], v[36:37], s[16:17] op_sel_hi:[1,0]
	ds_write_b128 v140, v[0:3]
	s_waitcnt vmcnt(22)
	v_pk_mul_f32 v[2:3], v[34:35], s[16:17] op_sel_hi:[1,0]
	v_pk_mul_f32 v[0:1], v[32:33], s[16:17] op_sel_hi:[1,0]
	ds_write_b128 v141, v[0:3]
	s_waitcnt vmcnt(21)
	v_pk_mul_f32 v[2:3], v[46:47], s[16:17] op_sel_hi:[1,0]
	v_pk_mul_f32 v[0:1], v[44:45], s[16:17] op_sel_hi:[1,0]
	ds_write_b128 v142, v[0:3]
	s_waitcnt vmcnt(20)
	v_pk_mul_f32 v[2:3], v[42:43], s[16:17] op_sel_hi:[1,0]
	v_pk_mul_f32 v[0:1], v[40:41], s[16:17] op_sel_hi:[1,0]
	ds_write_b128 v143, v[0:3]
	s_waitcnt vmcnt(19)
	v_pk_mul_f32 v[2:3], v[54:55], s[16:17] op_sel_hi:[1,0]
	v_pk_mul_f32 v[0:1], v[52:53], s[16:17] op_sel_hi:[1,0]
	ds_write_b128 v144, v[0:3]
	s_waitcnt vmcnt(18)
	v_pk_mul_f32 v[2:3], v[50:51], s[16:17] op_sel_hi:[1,0]
	v_pk_mul_f32 v[0:1], v[48:49], s[16:17] op_sel_hi:[1,0]
	ds_write_b128 v145, v[0:3]
	s_waitcnt vmcnt(17)
	v_pk_mul_f32 v[2:3], v[62:63], s[16:17] op_sel_hi:[1,0]
	v_pk_mul_f32 v[0:1], v[60:61], s[16:17] op_sel_hi:[1,0]
	ds_write_b128 v146, v[0:3]
	s_waitcnt vmcnt(16)
	v_pk_mul_f32 v[2:3], v[58:59], s[16:17] op_sel_hi:[1,0]
	v_pk_mul_f32 v[0:1], v[56:57], s[16:17] op_sel_hi:[1,0]
	ds_write_b128 v147, v[0:3]
	s_waitcnt lgkmcnt(0)
	ds_read2_b32 v[0:1], v148 offset1:32
	ds_read2_b32 v[8:9], v148 offset0:64 offset1:96
	s_add_u32 s8, s14, 0x4000
	s_waitcnt lgkmcnt(0)
	v_cvt_pk_fp8_f32 v4, v0, v1
	ds_read2_b32 v[0:1], v148 offset0:128 offset1:160
	ds_read2_b32 v[10:11], v148 offset0:192 offset1:224
	ds_read2_b32 v[12:13], v152 offset1:32
	s_waitcnt lgkmcnt(2)
	v_cvt_pk_fp8_f32 v5, v0, v1
	ds_read2_b32 v[0:1], v152 offset0:64 offset1:96
	ds_read2_b32 v[14:15], v152 offset0:128 offset1:160
	s_waitcnt lgkmcnt(2)
	v_cvt_pk_fp8_f32 v6, v12, v13
	ds_read2_b32 v[12:13], v152 offset0:192 offset1:224
	v_cvt_pk_fp8_f32 v4, v8, v9 op_sel:[0,0,1]
	s_waitcnt lgkmcnt(1)
	v_cvt_pk_fp8_f32 v7, v14, v15
	v_cvt_pk_fp8_f32 v5, v10, v11 op_sel:[0,0,1]
	v_cvt_pk_fp8_f32 v6, v0, v1 op_sel:[0,0,1]
	ds_read2_b32 v[0:1], v149 offset1:32
	s_waitcnt lgkmcnt(1)
	v_cvt_pk_fp8_f32 v7, v12, v13 op_sel:[0,0,1]
	v_lshl_add_u64 v[8:9], s[14:15], 0, v[128:129]
	s_addc_u32 s9, s15, 0
	v_add_u32_e32 v155, 0x400, v151
	global_store_dwordx4 v[8:9], v[4:7], off nt
	ds_read2_b32 v[8:9], v149 offset0:64 offset1:96
	s_waitcnt lgkmcnt(1)
	v_cvt_pk_fp8_f32 v4, v0, v1
	ds_read2_b32 v[0:1], v149 offset0:128 offset1:160
	ds_read2_b32 v[10:11], v149 offset0:192 offset1:224
	ds_read2_b32 v[12:13], v153 offset1:32
	s_waitcnt lgkmcnt(2)
	v_cvt_pk_fp8_f32 v5, v0, v1
	ds_read2_b32 v[0:1], v153 offset0:64 offset1:96
	ds_read2_b32 v[14:15], v153 offset0:128 offset1:160
	s_waitcnt lgkmcnt(2)
	v_cvt_pk_fp8_f32 v6, v12, v13
	ds_read2_b32 v[12:13], v153 offset0:192 offset1:224
	v_cvt_pk_fp8_f32 v4, v8, v9 op_sel:[0,0,1]
	s_waitcnt lgkmcnt(1)
	v_cvt_pk_fp8_f32 v7, v14, v15
	v_cvt_pk_fp8_f32 v5, v10, v11 op_sel:[0,0,1]
	v_cvt_pk_fp8_f32 v6, v0, v1 op_sel:[0,0,1]
	ds_read2_b32 v[0:1], v150 offset1:32
	s_waitcnt lgkmcnt(1)
	v_cvt_pk_fp8_f32 v7, v12, v13 op_sel:[0,0,1]
	v_lshl_add_u64 v[8:9], s[8:9], 0, v[128:129]
	s_add_u32 s8, s14, 0x8000
	s_addc_u32 s9, s15, 0
	global_store_dwordx4 v[8:9], v[4:7], off nt
	ds_read2_b32 v[8:9], v150 offset0:64 offset1:96
	s_nop 0
	s_waitcnt lgkmcnt(1)
	v_cvt_pk_fp8_f32 v4, v0, v1
	ds_read2_b32 v[0:1], v150 offset0:128 offset1:160
	ds_read2_b32 v[10:11], v150 offset0:192 offset1:224
	ds_read2_b32 v[12:13], v154 offset1:32
	s_waitcnt lgkmcnt(2)
	v_cvt_pk_fp8_f32 v5, v0, v1
	ds_read2_b32 v[0:1], v154 offset0:64 offset1:96
	ds_read2_b32 v[14:15], v154 offset0:128 offset1:160
	s_waitcnt lgkmcnt(2)
	v_cvt_pk_fp8_f32 v6, v12, v13
	ds_read2_b32 v[12:13], v154 offset0:192 offset1:224
	v_cvt_pk_fp8_f32 v4, v8, v9 op_sel:[0,0,1]
	s_waitcnt lgkmcnt(1)
	v_cvt_pk_fp8_f32 v7, v14, v15
	v_cvt_pk_fp8_f32 v5, v10, v11 op_sel:[0,0,1]
	v_cvt_pk_fp8_f32 v6, v0, v1 op_sel:[0,0,1]
	ds_read2_b32 v[8:9], v151 offset1:32
	s_waitcnt lgkmcnt(1)
	v_cvt_pk_fp8_f32 v7, v12, v13 op_sel:[0,0,1]
	v_lshl_add_u64 v[0:1], s[8:9], 0, v[128:129]
	s_add_u32 s8, s14, 0xc000
	s_addc_u32 s9, s15, 0
	global_store_dwordx4 v[0:1], v[4:7], off nt
	ds_read2_b32 v[4:5], v151 offset0:64 offset1:96
	s_waitcnt lgkmcnt(1)
	v_cvt_pk_fp8_f32 v0, v8, v9
	ds_read2_b32 v[6:7], v151 offset0:128 offset1:160
	ds_read2_b32 v[8:9], v151 offset0:192 offset1:224
	ds_read2_b32 v[10:11], v155 offset1:32
	s_waitcnt lgkmcnt(3)
	v_cvt_pk_fp8_f32 v0, v4, v5 op_sel:[0,0,1]
	s_waitcnt lgkmcnt(2)
	v_cvt_pk_fp8_f32 v1, v6, v7
	ds_read2_b32 v[6:7], v155 offset0:128 offset1:160
	ds_read2_b32 v[12:13], v155 offset0:64 offset1:96
	s_waitcnt lgkmcnt(2)
	v_cvt_pk_fp8_f32 v2, v10, v11
	ds_read2_b32 v[10:11], v155 offset0:192 offset1:224
	v_cvt_pk_fp8_f32 v1, v8, v9 op_sel:[0,0,1]
	s_waitcnt lgkmcnt(2)
	v_cvt_pk_fp8_f32 v3, v6, v7
	s_waitcnt lgkmcnt(1)
	v_cvt_pk_fp8_f32 v2, v12, v13 op_sel:[0,0,1]
	v_lshl_add_u64 v[4:5], s[8:9], 0, v[128:129]
	s_andn2_b64 vcc, exec, s[20:21]
	s_waitcnt lgkmcnt(0)
	v_cvt_pk_fp8_f32 v3, v10, v11 op_sel:[0,0,1]
	s_mov_b64 s[20:21], -1
	global_store_dwordx4 v[4:5], v[0:3], off nt
	s_waitcnt lgkmcnt(0)
	s_cbranch_vccnz .LBB0_558
	s_add_i32 s1, s0, s1
	s_cmp_lt_i32 s1, s45
	s_cselect_b32 s1, s1, s3
	s_cmp_lt_i32 s1, 0x10000
	s_cselect_b64 s[14:15], -1, 0
	s_cmp_gt_i32 s1, 0xffff
	s_mov_b64 s[24:25], -1
	s_cbranch_scc0 .LBB0_567
	s_add_i32 s8, s1, 0xffff0000
	s_lshr_b32 s12, s8, 10
	s_and_b32 s9, s1, 0x3ff
	s_lshl_b64 s[20:21], s[12:13], 22
	s_lshl_b64 s[22:23], s[12:13], 24
	s_add_u32 s22, s6, s22
	s_addc_u32 s23, s7, s23
	s_add_u32 s20, s77, s20
	v_readlane_b32 s8, v252, 33
	s_addc_u32 s21, s8, s21
	s_mov_b64 s[24:25], 0

; __device__ __forceinline__ void mask_tile(f32x16& p0, f32x16& p1, int dq, unsigned W) {
;     const float NEG = -__builtin_inff();
; #pragma unroll
;     for (int r = 0; r < 16; ++r) {
;         const int c = (r & 3) + 8 * (r >> 2);
;         if ((unsigned)(dq - c) >= W) p0[r] = NEG;
;         if ((unsigned)(dq - c - 32) >= W) p1[r] = NEG;
;     }
; }
; template <bool FIRST>
; __device__ __forceinline__ bool partialSM(f32x16& p0, f32x16& p1, float& M, f32x16& minit, float& alpha) {
;     float tmax = p0[0]; for (int r = 1; r < 16; ++r) tmax = fmaxf(tmax, p0[r]); for (int r = 0; r < 16; ++r) tmax = fmaxf(tmax, p1[r]);
;     { auto rr = __builtin_amdgcn_permlane32_swap(__float_as_uint(tmax), __float_as_uint(tmax), false, false);
;       tmax = fmaxf(__uint_as_float(rr[0]), __uint_as_float(rr[1])); }
;     const float d0 = tmax - PLOG2;
;     const bool moved = FIRST || !__all(d0 <= THR * 1.4426950408889634f);
;     if (__builtin_expect(moved, FIRST)) {
;         const float d = FIRST ? d0 : fmaxf(d0, 0.f);
;         alpha = __builtin_amdgcn_exp2f(-d); M += d;
;         for (int r = 0; r < 16; ++r) { p0[r] -= d; p1[r] -= d; }
;         const float mi = PLOG2 - M;
;         for (int r = 0; r < 16; ++r) minit[r] = mi;
;     } else alpha = 1.f;
;     for (int r = 0; r < 16; ++r) p0[r] = __builtin_amdgcn_exp2f(p0[r]);
;     return moved;
; }
; __device__ __forceinline__ void finishSM(f32x16& p0, f32x16& p1, i32x8& pa) {
;     for (int r = 0; r < 16; ++r) p1[r] = __builtin_amdgcn_exp2f(p1[r]);
; #pragma unroll
;     for (int v = 0; v < 4; ++v) { pa[v] = (int)cvt_pk4_fp8(p0[4 * v], p0[4 * v + 1], p0[4 * v + 2], p0[4 * v + 3]); pa[4 + v] = (int)cvt_pk4_fp8(p1[4 * v], p1[4 * v + 1], p1[4 * v + 2], p1[4 * v + 3]); }
; }
; __device__ __forceinline__ void qkt(f32x16& p0, f32x16& p1, const char* stg, int ka, const i32x8* qf, const f32x16& minit) {
;     p0 = minit; p1 = minit;
; #pragma unroll
;     for (int s = 0; s < 3; ++s) { const char* a = stg + SOFF_K + s * 4096 + ka; const char* b = stg + SOFF_K + s * 4096 + (ka ^ 16);
;         const i32x4 a0 = *reinterpret_cast<const i32x4*>(a), a1 = *reinterpret_cast<const i32x4*>(b);
;         const i32x4 c0 = *reinterpret_cast<const i32x4*>(a + 2048), c1 = *reinterpret_cast<const i32x4*>(b + 2048);
.LBB0_594:
	s_cmp_gt_i32 s0, 4
	s_cselect_b32 s46, -5, 1
	s_add_i32 s46, s46, s0
	s_mulk_i32 s46, 0x5000
	s_add_i32 s46, s46, 0
	v_add_u32_e32 v199, s46, v192
	v_add_u32_e32 v200, s46, v193
	ds_read_b128 v[112:115], v199
	ds_read_b128 v[116:119], v200
	ds_read_b128 v[220:223], v199 offset:2048
	ds_read_b128 v[224:227], v200 offset:2048
	ds_read_b128 v[236:239], v199 offset:4096
	ds_read_b128 v[240:243], v200 offset:4096
	ds_read_b128 v[244:247], v199 offset:6144
	ds_read_b128 v[248:251], v200 offset:6144
	v_exp_f32_e32 v201, v96
	s_waitcnt lgkmcnt(6)
	v_mfma_f32_32x32x64_f8f6f4 v[128:143], v[112:119], v[168:175], v[80:95]
	v_exp_f32_e32 v97, v97
	v_exp_f32_e32 v202, v100
	v_exp_f32_e32 v219, v101
	v_exp_f32_e32 v98, v98
	v_exp_f32_e32 v99, v99
	v_exp_f32_e32 v102, v102
	v_exp_f32_e32 v104, v104
	v_exp_f32_e32 v105, v105
	v_exp_f32_e32 v108, v108
	v_exp_f32_e32 v109, v109
	v_exp_f32_e32 v106, v106
	v_exp_f32_e32 v107, v107
	v_exp_f32_e32 v110, v110
	v_exp_f32_e32 v111, v111
	s_waitcnt lgkmcnt(4)
	v_mfma_f32_32x32x64_f8f6f4 v[112:127], v[220:227], v[168:175], v[80:95]
	ds_read_b128 v[220:223], v199 offset:8192
	ds_read_b128 v[224:227], v200 offset:8192
	ds_read_b128 v[228:231], v199 offset:10240
	ds_read_b128 v[232:235], v200 offset:10240
	s_waitcnt lgkmcnt(6)
	v_mfma_f32_32x32x64_f8f6f4 v[128:143], v[236:243], v[176:183], v[128:143]
	s_waitcnt lgkmcnt(4)
	v_mfma_f32_32x32x64_f8f6f4 v[112:127], v[244:251], v[176:183], v[112:127]
	s_mul_i32 s98, s0, 0x5000
	v_add_u32_e32 v253, s98, v192
	v_add_u32_e32 v254, s98, v193
	ds_read_b128 v[240:243], v254 offset:12288
	ds_read_b128 v[236:239], v253 offset:12288
	ds_read_b128 v[244:247], v253 offset:14336
	ds_read_b128 v[248:251], v254 offset:14336
	s_waitcnt lgkmcnt(6)
	v_mfma_f32_32x32x64_f8f6f4 v[128:143], v[220:227], v[160:167], v[128:143]
	v_exp_f32_e32 v220, v103
	s_nop 0
	v_cvt_pk_fp8_f32 v100, v201, v97
	v_cvt_pk_fp8_f32 v101, v202, v219
	v_cvt_pk_fp8_f32 v100, v98, v99 op_sel:[0,0,1]
	v_cvt_pk_fp8_f32 v101, v102, v220 op_sel:[0,0,1]
	v_cvt_pk_fp8_f32 v96, v217, v218
	s_waitcnt lgkmcnt(4)
	v_mfma_f32_32x32x64_f8f6f4 v[112:127], v[228:235], v[160:167], v[112:127]
	v_cvt_pk_fp8_f32 v97, v213, v214
	v_cvt_pk_fp8_f32 v98, v209, v210
	v_cvt_pk_fp8_f32 v102, v104, v105
	v_cvt_pk_fp8_f32 v99, v205, v206
	v_cvt_pk_fp8_f32 v103, v108, v109
	v_cvt_pk_fp8_f32 v96, v215, v216 op_sel:[0,0,1]
	v_cvt_pk_fp8_f32 v97, v211, v212 op_sel:[0,0,1]
	v_cvt_pk_fp8_f32 v98, v207, v208 op_sel:[0,0,1]
	v_cvt_pk_fp8_f32 v102, v106, v107 op_sel:[0,0,1]
	v_cvt_pk_fp8_f32 v99, v203, v204 op_sel:[0,0,1]
	v_cvt_pk_fp8_f32 v103, v110, v111 op_sel:[0,0,1]
	s_mul_i32 s46, s0, 0x5000
	s_add_i32 s46, s46, 0
	v_add_u32_e32 v202, s46, v193
	v_add_u32_e32 v201, s46, v192
	ds_read_b128 v[108:111], v202 offset:16384
	ds_read_b128 v[104:107], v201 offset:16384
	v_mfma_f32_32x32x64_f8f6f4 v[64:79], v[96:103], v[152:159], v[64:79]
	s_sub_i32 s46, s1, 64
	s_cmp_le_u32 s46, s39
	s_waitcnt lgkmcnt(4)
	v_mfma_f32_32x32x64_f8f6f4 v[48:63], v[96:103], v[236:243], v[48:63]
	ds_read_b128 v[236:239], v201 offset:18432
	ds_read_b128 v[240:243], v202 offset:18432
	s_waitcnt lgkmcnt(4)
	v_mfma_f32_32x32x64_f8f6f4 v[0:15], v[96:103], v[244:251], v[0:15]
	s_waitcnt lgkmcnt(2)
	v_mfma_f32_32x32x64_f8f6f4 v[32:47], v[96:103], v[104:111], v[32:47]
	s_waitcnt lgkmcnt(0)
	v_mfma_f32_32x32x64_f8f6f4 v[16:31], v[96:103], v[236:243], v[16:31]
	s_cbranch_scc1 .LBB0_596
	v_add_u32_e32 v96, 0x4000007b, v198
	v_cmp_gt_u32_e32 vcc, 2.0, v96
	v_add_u32_e32 v96, 0x5b, v198
	s_nop 0
	v_cndmask_b32_e32 v128, v187, v128, vcc
	v_cmp_lt_u32_e32 vcc, s37, v96
	v_add_u32_e32 v96, 0x7a, v198
	s_nop 0
	v_cndmask_b32_e32 v112, v187, v112, vcc
	v_cmp_lt_u32_e32 vcc, s37, v96
	v_add_u32_e32 v96, 0x5a, v198
	s_nop 0
	v_cndmask_b32_e32 v129, v187, v129, vcc
	v_cmp_lt_u32_e32 vcc, s37, v96
	v_add_u32_e32 v96, 0x79, v198
	s_nop 0
	v_cndmask_b32_e32 v113, v187, v113, vcc
	v_cmp_lt_u32_e32 vcc, s37, v96
	v_add_u32_e32 v96, 0x59, v198
	s_nop 0
	v_cndmask_b32_e32 v130, v187, v130, vcc
	v_cmp_lt_u32_e32 vcc, s37, v96
	v_add_u32_e32 v96, 0x78, v198
	s_nop 0
	v_cndmask_b32_e32 v114, v187, v114, vcc
	v_cmp_lt_u32_e32 vcc, s37, v96
	v_add_u32_e32 v96, 0x58, v198
	s_nop 0
	v_cndmask_b32_e32 v131, v187, v131, vcc
	v_cmp_lt_u32_e32 vcc, s37, v96
	v_add_u32_e32 v96, 0x73, v198
	s_nop 0
	v_cndmask_b32_e32 v115, v187, v115, vcc
	v_cmp_lt_u32_e32 vcc, s37, v96
	v_add_u32_e32 v96, 0x53, v198
	s_nop 0
	v_cndmask_b32_e32 v132, v187, v132, vcc
	v_cmp_lt_u32_e32 vcc, s37, v96
	v_add_u32_e32 v96, 0x72, v198
	s_nop 0
	v_cndmask_b32_e32 v116, v187, v116, vcc
	v_cmp_lt_u32_e32 vcc, s37, v96
	v_add_u32_e32 v96, 0x52, v198
	s_nop 0
	v_cndmask_b32_e32 v133, v187, v133, vcc
	v_cmp_lt_u32_e32 vcc, s37, v96
	v_add_u32_e32 v96, 0x71, v198
	s_nop 0
	v_cndmask_b32_e32 v117, v187, v117, vcc
	v_cmp_lt_u32_e32 vcc, s37, v96
	v_add_u32_e32 v96, 0x51, v198
	s_nop 0
	v_cndmask_b32_e32 v134, v187, v134, vcc
	v_cmp_lt_u32_e32 vcc, s37, v96
	v_add_u32_e32 v96, 0x70, v198
	s_nop 0
	v_cndmask_b32_e32 v118, v187, v118, vcc
	v_cmp_lt_u32_e32 vcc, s37, v96
	v_add_u32_e32 v96, 0x50, v198
	s_nop 0
	v_cndmask_b32_e32 v135, v187, v135, vcc
	v_cmp_lt_u32_e32 vcc, s37, v96
	v_add_u32_e32 v96, 0x6b, v198
	s_nop 0
	v_cndmask_b32_e32 v119, v187, v119, vcc
	v_cmp_lt_u32_e32 vcc, s37, v96
	v_add_u32_e32 v96, 0x4b, v198
	s_nop 0
	v_cndmask_b32_e32 v136, v187, v136, vcc
	v_cmp_lt_u32_e32 vcc, s37, v96
	v_add_u32_e32 v96, 0x6a, v198
	s_nop 0
	v_cndmask_b32_e32 v120, v187, v120, vcc
	v_cmp_lt_u32_e32 vcc, s37, v96
	v_add_u32_e32 v96, 0x4a, v198
	s_nop 0
	v_cndmask_b32_e32 v137, v187, v137, vcc
	v_cmp_lt_u32_e32 vcc, s37, v96
	v_add_u32_e32 v96, 0x69, v198
	s_nop 0
	v_cndmask_b32_e32 v121, v187, v121, vcc
	v_cmp_lt_u32_e32 vcc, s37, v96
	v_add_u32_e32 v96, 0x49, v198
	s_nop 0
	v_cndmask_b32_e32 v138, v187, v138, vcc
	v_cmp_lt_u32_e32 vcc, s37, v96
	v_add_u32_e32 v96, 0x68, v198
	s_nop 0
	v_cndmask_b32_e32 v122, v187, v122, vcc
	v_cmp_lt_u32_e32 vcc, s37, v96
	v_add_u32_e32 v96, 0x48, v198
	s_nop 0
	v_cndmask_b32_e32 v139, v187, v139, vcc
	v_cmp_lt_u32_e32 vcc, s37, v96
	v_add_u32_e32 v96, 0x63, v198
	s_nop 0
	v_cndmask_b32_e32 v123, v187, v123, vcc
	v_cmp_lt_u32_e32 vcc, s37, v96
	v_add_u32_e32 v96, 0x43, v198
	s_nop 0
	v_cndmask_b32_e32 v140, v187, v140, vcc
	v_cmp_lt_u32_e32 vcc, s37, v96
	v_add_u32_e32 v96, 0x62, v198
	s_nop 0
	v_cndmask_b32_e32 v124, v187, v124, vcc
	v_cmp_lt_u32_e32 vcc, s37, v96
	v_add_u32_e32 v96, 0x42, v198
	s_nop 0
	v_cndmask_b32_e32 v141, v187, v141, vcc
	v_cmp_lt_u32_e32 vcc, s37, v96
	v_add_u32_e32 v96, 0x61, v198
	s_nop 0
	v_cndmask_b32_e32 v125, v187, v125, vcc
	v_cmp_lt_u32_e32 vcc, s37, v96
	v_add_u32_e32 v96, 0x41, v198
	s_nop 0
	v_cndmask_b32_e32 v142, v187, v142, vcc
	v_cmp_lt_u32_e32 vcc, s37, v96
	v_add_u32_e32 v96, 0x60, v198
	s_nop 0
	v_cndmask_b32_e32 v126, v187, v126, vcc
	v_cmp_lt_u32_e32 vcc, s37, v96
	v_add_u32_e32 v96, 64, v198
	s_nop 0
	v_cndmask_b32_e32 v143, v187, v143, vcc
	v_cmp_lt_u32_e32 vcc, s37, v96
	s_nop 1
	v_cndmask_b32_e32 v127, v187, v127, vcc

; __device__ __forceinline__ unsigned cvt_pk4_fp8(float a, float b, float c, float d) { int w; asm("" : "=v"(w));     w = __builtin_amdgcn_cvt_pk_fp8_f32(a, b, w, false); w = __builtin_amdgcn_cvt_pk_fp8_f32(c, d, w, true); return (unsigned)w; }
; __device__ __forceinline__ void finishSM(f32x16& p0, f32x16& p1, i32x8& pa) {
;     for (int r = 0; r < 16; ++r) p1[r] = __builtin_amdgcn_exp2f(p1[r]);
; #pragma unroll
;     for (int v = 0; v < 4; ++v) { pa[v] = (int)cvt_pk4_fp8(p0[4 * v], p0[4 * v + 1], p0[4 * v + 2], p0[4 * v + 3]); pa[4 + v] = (int)cvt_pk4_fp8(p1[4 * v], p1[4 * v + 1], p1[4 * v + 2], p1[4 * v + 3]); }
; }
; __device__ __forceinline__ void qkt(f32x16& p0, f32x16& p1, const char* stg, int ka, const i32x8* qf, const f32x16& minit) {
;     p0 = minit; p1 = minit;
; #pragma unroll
;     for (int s = 0; s < 3; ++s) { const char* a = stg + SOFF_K + s * 4096 + ka; const char* b = stg + SOFF_K + s * 4096 + (ka ^ 16);
;         const i32x4 a0 = *reinterpret_cast<const i32x4*>(a), a1 = *reinterpret_cast<const i32x4*>(b);
;         const i32x4 c0 = *reinterpret_cast<const i32x4*>(a + 2048), c1 = *reinterpret_cast<const i32x4*>(b + 2048);
;         p0 = __builtin_amdgcn_mfma_scale_f32_32x32x64_f8f6f4(__builtin_shufflevector(a0, a1, 0, 1, 2, 3, 4, 5, 6, 7), qf[s], p0, 0, 0, 0, 0, 0, 0);
;         p1 = __builtin_amdgcn_mfma_scale_f32_32x32x64_f8f6f4(__builtin_shufflevector(c0, c1, 0, 1, 2, 3, 4, 5, 6, 7), qf[s], p1, 0, 0, 0, 0, 0, 0); }
; }
; __device__ __forceinline__ void v_read(i32x8 (&vf)[4], const char* stg, int ka) {
; #pragma unroll
;     for (int d0 = 0; d0 < 4; ++d0) { const i32x4 a0 = *reinterpret_cast<const i32x4*>(stg + SOFF_V + d0 * 2048 + ka), a1 = *reinterpret_cast<const i32x4*>(stg + SOFF_V + d0 * 2048 + (ka ^ 16));
;         vf[d0] = __builtin_shufflevector(a0, a1, 0, 1, 2, 3, 4, 5, 6, 7); }
; }
; __device__ __forceinline__ void pv_mma(f32x16* o, f32x16& ol, const i32x8 (&vf)[4], const i32x8 ones, const i32x8 pa) {
; #pragma unroll
;     for (int d0 = 0; d0 < 4; ++d0) o[d0] = __builtin_amdgcn_mfma_scale_f32_32x32x64_f8f6f4(pa, vf[d0], o[d0], 0, 0, 0, 0, 0, 0);
;     ol = __builtin_amdgcn_mfma_scale_f32_32x32x64_f8f6f4(pa, ones, ol, 0, 0, 0, 0, 0, 0);
; }
.LBB0_601:
	s_cmp_gt_i32 s0, 3
	s_cselect_b32 s46, -4, 2
	s_add_i32 s0, s46, s0
	v_exp_f32_e32 v203, v128
	v_exp_f32_e32 v220, v129
	v_exp_f32_e32 v221, v130
	v_exp_f32_e32 v222, v131
	v_exp_f32_e32 v223, v132
	v_exp_f32_e32 v224, v133
	v_exp_f32_e32 v225, v134
	v_exp_f32_e32 v226, v135
	v_exp_f32_e32 v227, v136
	v_exp_f32_e32 v228, v137
	v_exp_f32_e32 v229, v138
	v_exp_f32_e32 v230, v139
	v_exp_f32_e32 v231, v140
	v_exp_f32_e32 v232, v141
	v_exp_f32_e32 v233, v142
	v_exp_f32_e32 v234, v143
	s_mul_i32 s46, s0, 0x5000
	s_add_i32 s46, s46, 0
	v_add_u32_e32 v202, s46, v192
	v_add_u32_e32 v201, s46, v193
	ds_read_b128 v[204:207], v202
	ds_read_b128 v[208:211], v201
	ds_read_b128 v[212:215], v202 offset:2048
	ds_read_b128 v[216:219], v201 offset:2048
	ds_read_b128 v[236:239], v202 offset:4096
	ds_read_b128 v[240:243], v201 offset:4096
	ds_read_b128 v[244:247], v202 offset:6144
	ds_read_b128 v[248:251], v201 offset:6144
	v_exp_f32_e32 v113, v113
	s_waitcnt lgkmcnt(6)
	v_mfma_f32_32x32x64_f8f6f4 v[128:143], v[204:211], v[168:175], v[96:111]
	v_exp_f32_e32 v114, v114
	v_exp_f32_e32 v115, v115
	v_exp_f32_e32 v118, v118
	v_exp_f32_e32 v120, v120
	v_exp_f32_e32 v121, v121
	v_exp_f32_e32 v124, v124
	v_exp_f32_e32 v125, v125
	v_exp_f32_e32 v122, v122
	v_exp_f32_e32 v123, v123
	v_exp_f32_e32 v126, v126
	v_exp_f32_e32 v127, v127
	s_waitcnt lgkmcnt(4)
	v_mfma_f32_32x32x64_f8f6f4 v[96:111], v[212:219], v[168:175], v[96:111]
	ds_read_b128 v[204:207], v202 offset:8192
	ds_read_b128 v[208:211], v201 offset:8192
	ds_read_b128 v[212:215], v202 offset:10240
	ds_read_b128 v[216:219], v201 offset:10240
	s_waitcnt lgkmcnt(6)
	v_mfma_f32_32x32x64_f8f6f4 v[128:143], v[236:243], v[176:183], v[128:143]
	s_waitcnt lgkmcnt(4)
	v_mfma_f32_32x32x64_f8f6f4 v[96:111], v[244:251], v[176:183], v[96:111]
	ds_read_b128 v[240:243], v200 offset:12288
	ds_read_b128 v[236:239], v199 offset:12288
	ds_read_b128 v[244:247], v199 offset:14336
	ds_read_b128 v[248:251], v200 offset:14336
	s_waitcnt lgkmcnt(6)
	v_mfma_f32_32x32x64_f8f6f4 v[128:143], v[204:211], v[160:167], v[128:143]
	v_exp_f32_e32 v204, v112
	v_exp_f32_e32 v205, v116
	v_exp_f32_e32 v206, v117
	v_exp_f32_e32 v207, v119
	s_nop 0
	v_cvt_pk_fp8_f32 v116, v204, v113
	v_cvt_pk_fp8_f32 v117, v205, v206
	v_cvt_pk_fp8_f32 v116, v114, v115 op_sel:[0,0,1]
	v_cvt_pk_fp8_f32 v117, v118, v207 op_sel:[0,0,1]
	s_waitcnt lgkmcnt(4)
	v_mfma_f32_32x32x64_f8f6f4 v[96:111], v[212:219], v[160:167], v[96:111]
	v_cvt_pk_fp8_f32 v112, v203, v220
	v_cvt_pk_fp8_f32 v113, v223, v224
	v_cvt_pk_fp8_f32 v114, v227, v228
	v_cvt_pk_fp8_f32 v118, v120, v121
	v_cvt_pk_fp8_f32 v115, v231, v232
	v_cvt_pk_fp8_f32 v119, v124, v125
	v_cvt_pk_fp8_f32 v112, v221, v222 op_sel:[0,0,1]
	v_cvt_pk_fp8_f32 v113, v225, v226 op_sel:[0,0,1]
	v_cvt_pk_fp8_f32 v114, v229, v230 op_sel:[0,0,1]
	v_cvt_pk_fp8_f32 v118, v122, v123 op_sel:[0,0,1]
	v_cvt_pk_fp8_f32 v115, v233, v234 op_sel:[0,0,1]
	v_cvt_pk_fp8_f32 v119, v126, v127 op_sel:[0,0,1]
	ds_read_b128 v[124:127], v200 offset:16384
	ds_read_b128 v[120:123], v199 offset:16384
	v_mfma_f32_32x32x64_f8f6f4 v[64:79], v[112:119], v[152:159], v[64:79]
	s_cmp_le_u32 s1, s39
	s_waitcnt lgkmcnt(4)
	v_mfma_f32_32x32x64_f8f6f4 v[48:63], v[112:119], v[236:243], v[48:63]
	ds_read_b128 v[236:239], v199 offset:18432
	ds_read_b128 v[240:243], v200 offset:18432
	s_waitcnt lgkmcnt(4)
	v_mfma_f32_32x32x64_f8f6f4 v[0:15], v[112:119], v[244:251], v[0:15]
	s_waitcnt lgkmcnt(2)
	v_mfma_f32_32x32x64_f8f6f4 v[32:47], v[112:119], v[120:127], v[32:47]
	s_waitcnt lgkmcnt(0)
	v_mfma_f32_32x32x64_f8f6f4 v[16:31], v[112:119], v[236:243], v[16:31]
	s_cbranch_scc1 .LBB0_603
; __device__ __forceinline__ void mask_tile(f32x16& p0, f32x16& p1, int dq, unsigned W) {
;     const float NEG = -__builtin_inff();
; #pragma unroll
;     for (int r = 0; r < 16; ++r) {
;         const int c = (r & 3) + 8 * (r >> 2);
;         if ((unsigned)(dq - c) >= W) p0[r] = NEG;
;         if ((unsigned)(dq - c - 32) >= W) p1[r] = NEG;
;     }
; }
	v_add_u32_e32 v112, 0x4000003b, v198
	v_cmp_gt_u32_e32 vcc, 2.0, v112
	v_add_u32_e32 v112, 27, v198
	s_nop 0
	v_cndmask_b32_e32 v128, v187, v128, vcc
	v_cmp_lt_u32_e32 vcc, s37, v112
	v_add_u32_e32 v112, 58, v198
	s_nop 0
	v_cndmask_b32_e32 v96, v187, v96, vcc
	v_cmp_lt_u32_e32 vcc, s37, v112
	v_add_u32_e32 v112, 26, v198
	s_nop 0
	v_cndmask_b32_e32 v129, v187, v129, vcc
	v_cmp_lt_u32_e32 vcc, s37, v112
	v_add_u32_e32 v112, 57, v198
	s_nop 0
	v_cndmask_b32_e32 v97, v187, v97, vcc
	v_cmp_lt_u32_e32 vcc, s37, v112
	v_add_u32_e32 v112, 25, v198
	s_nop 0
	v_cndmask_b32_e32 v130, v187, v130, vcc
	v_cmp_lt_u32_e32 vcc, s37, v112
	v_add_u32_e32 v112, 56, v198
	s_nop 0
	v_cndmask_b32_e32 v98, v187, v98, vcc
	v_cmp_lt_u32_e32 vcc, s37, v112
	v_add_u32_e32 v112, 24, v198
	s_nop 0
	v_cndmask_b32_e32 v131, v187, v131, vcc
	v_cmp_lt_u32_e32 vcc, s37, v112
	v_add_u32_e32 v112, 51, v198
	s_nop 0
	v_cndmask_b32_e32 v99, v187, v99, vcc
	v_cmp_lt_u32_e32 vcc, s37, v112
	v_add_u32_e32 v112, 19, v198
	s_nop 0
	v_cndmask_b32_e32 v132, v187, v132, vcc
	v_cmp_lt_u32_e32 vcc, s37, v112
	v_add_u32_e32 v112, 50, v198
	s_nop 0
	v_cndmask_b32_e32 v100, v187, v100, vcc
	v_cmp_lt_u32_e32 vcc, s37, v112
	v_add_u32_e32 v112, 18, v198
	s_nop 0
	v_cndmask_b32_e32 v133, v187, v133, vcc
	v_cmp_lt_u32_e32 vcc, s37, v112
	v_add_u32_e32 v112, 49, v198
	s_nop 0
	v_cndmask_b32_e32 v101, v187, v101, vcc
	v_cmp_lt_u32_e32 vcc, s37, v112
	v_add_u32_e32 v112, 17, v198
	s_nop 0
	v_cndmask_b32_e32 v134, v187, v134, vcc
	v_cmp_lt_u32_e32 vcc, s37, v112
	v_add_u32_e32 v112, 48, v198
	s_nop 0
	v_cndmask_b32_e32 v102, v187, v102, vcc
	v_cmp_lt_u32_e32 vcc, s37, v112
	v_add_u32_e32 v112, 16, v198
	s_nop 0
	v_cndmask_b32_e32 v135, v187, v135, vcc
	v_cmp_lt_u32_e32 vcc, s37, v112
	v_add_u32_e32 v112, 43, v198
	s_nop 0
	v_cndmask_b32_e32 v103, v187, v103, vcc
	v_cmp_lt_u32_e32 vcc, s37, v112
	v_add_u32_e32 v112, 11, v198
	s_nop 0
	v_cndmask_b32_e32 v136, v187, v136, vcc
	v_cmp_lt_u32_e32 vcc, s37, v112
	v_add_u32_e32 v112, 42, v198
	s_nop 0
	v_cndmask_b32_e32 v104, v187, v104, vcc
	v_cmp_lt_u32_e32 vcc, s37, v112
	v_add_u32_e32 v112, 10, v198
	s_nop 0
	v_cndmask_b32_e32 v137, v187, v137, vcc
	v_cmp_lt_u32_e32 vcc, s37, v112
	v_add_u32_e32 v112, 41, v198
	s_nop 0
	v_cndmask_b32_e32 v105, v187, v105, vcc
	v_cmp_lt_u32_e32 vcc, s37, v112
	v_add_u32_e32 v112, 9, v198
	s_nop 0
	v_cndmask_b32_e32 v138, v187, v138, vcc
	v_cmp_lt_u32_e32 vcc, s37, v112
	v_add_u32_e32 v112, 40, v198
	s_nop 0
	v_cndmask_b32_e32 v106, v187, v106, vcc
	v_cmp_lt_u32_e32 vcc, s37, v112
	v_add_u32_e32 v112, 8, v198
	s_nop 0
	v_cndmask_b32_e32 v139, v187, v139, vcc
	v_cmp_lt_u32_e32 vcc, s37, v112
	v_add_u32_e32 v112, 35, v198
	s_nop 0
	v_cndmask_b32_e32 v107, v187, v107, vcc
	v_cmp_lt_u32_e32 vcc, s37, v112
	v_add_u32_e32 v112, 3, v198
	s_nop 0
	v_cndmask_b32_e32 v140, v187, v140, vcc
	v_cmp_lt_u32_e32 vcc, s37, v112
	v_add_u32_e32 v112, 34, v198
	s_nop 0
	v_cndmask_b32_e32 v108, v187, v108, vcc
	v_cmp_lt_u32_e32 vcc, s37, v112
	v_add_u32_e32 v112, 2, v198
	s_nop 0
	v_cndmask_b32_e32 v141, v187, v141, vcc
	v_cmp_lt_u32_e32 vcc, s37, v112
	v_add_u32_e32 v112, 33, v198
	s_nop 0
	v_cndmask_b32_e32 v109, v187, v109, vcc
	v_cmp_lt_u32_e32 vcc, s37, v112
	v_add_u32_e32 v112, 1, v198
	s_nop 0
	v_cndmask_b32_e32 v142, v187, v142, vcc
	v_cmp_lt_u32_e32 vcc, s37, v112
	v_add_u32_e32 v112, 32, v198
	s_nop 0
	v_cndmask_b32_e32 v110, v187, v110, vcc
	v_cmp_lt_u32_e32 vcc, s37, v112
	s_nop 1
	v_cndmask_b32_e32 v143, v187, v143, vcc
	v_cmp_lt_u32_e32 vcc, s37, v198
	s_nop 1
	v_cndmask_b32_e32 v111, v187, v111, vcc

; __device__ __forceinline__ void mask_tile(f32x16& p0, f32x16& p1, int dq, unsigned W) {
;     const float NEG = -__builtin_inff();
; #pragma unroll
;     for (int r = 0; r < 16; ++r) {
;         const int c = (r & 3) + 8 * (r >> 2);
;         if ((unsigned)(dq - c) >= W) p0[r] = NEG;
;         if ((unsigned)(dq - c - 32) >= W) p1[r] = NEG;
;     }
; }
; template <bool FIRST>
; __device__ __forceinline__ bool partialSM(f32x16& p0, f32x16& p1, float& M, f32x16& minit, float& alpha) {
;     float tmax = p0[0]; for (int r = 1; r < 16; ++r) tmax = fmaxf(tmax, p0[r]); for (int r = 0; r < 16; ++r) tmax = fmaxf(tmax, p1[r]);
;     { auto rr = __builtin_amdgcn_permlane32_swap(__float_as_uint(tmax), __float_as_uint(tmax), false, false);
;       tmax = fmaxf(__uint_as_float(rr[0]), __uint_as_float(rr[1])); }
;     const float d0 = tmax - PLOG2;
;     const bool moved = FIRST || !__all(d0 <= THR * 1.4426950408889634f);
;     if (__builtin_expect(moved, FIRST)) {
;         const float d = FIRST ? d0 : fmaxf(d0, 0.f);
;         alpha = __builtin_amdgcn_exp2f(-d); M += d;
;         for (int r = 0; r < 16; ++r) { p0[r] -= d; p1[r] -= d; }
;         const float mi = PLOG2 - M;
;         for (int r = 0; r < 16; ++r) minit[r] = mi;
;     } else alpha = 1.f;
;     for (int r = 0; r < 16; ++r) p0[r] = __builtin_amdgcn_exp2f(p0[r]);
;     return moved;
; }
; __device__ __forceinline__ void finishSM(f32x16& p0, f32x16& p1, i32x8& pa) {
;     for (int r = 0; r < 16; ++r) p1[r] = __builtin_amdgcn_exp2f(p1[r]);
; #pragma unroll
;     for (int v = 0; v < 4; ++v) { pa[v] = (int)cvt_pk4_fp8(p0[4 * v], p0[4 * v + 1], p0[4 * v + 2], p0[4 * v + 3]); pa[4 + v] = (int)cvt_pk4_fp8(p1[4 * v], p1[4 * v + 1], p1[4 * v + 2], p1[4 * v + 3]); }
; }
; __device__ __forceinline__ void qkt(f32x16& p0, f32x16& p1, const char* stg, int ka, const i32x8* qf, const f32x16& minit) {
;     p0 = minit; p1 = minit;
; #pragma unroll
;     for (int s = 0; s < 3; ++s) { const char* a = stg + SOFF_K + s * 4096 + ka; const char* b = stg + SOFF_K + s * 4096 + (ka ^ 16);
;         const i32x4 a0 = *reinterpret_cast<const i32x4*>(a), a1 = *reinterpret_cast<const i32x4*>(b);
;         const i32x4 c0 = *reinterpret_cast<const i32x4*>(a + 2048), c1 = *reinterpret_cast<const i32x4*>(b + 2048);
.LBB0_667:
	s_cmp_gt_i32 s1, 4
	s_cselect_b32 s46, -5, 1
	s_add_i32 s46, s46, s1
	s_mulk_i32 s46, 0x5000
	s_add_i32 s46, s46, 0
	v_add_u32_e32 v199, s46, v193
	v_add_u32_e32 v200, s46, v194
	ds_read_b128 v[112:115], v199
	ds_read_b128 v[116:119], v200
	ds_read_b128 v[218:221], v199 offset:2048
	ds_read_b128 v[222:225], v200 offset:2048
	ds_read_b128 v[236:239], v199 offset:4096
	ds_read_b128 v[240:243], v200 offset:4096
	ds_read_b128 v[244:247], v199 offset:6144
	ds_read_b128 v[248:251], v200 offset:6144
	v_exp_f32_e32 v217, v96
	s_waitcnt lgkmcnt(6)
	v_mfma_f32_32x32x64_f8f6f4 v[128:143], v[112:119], v[168:175], v[80:95]
	v_exp_f32_e32 v97, v97
	v_exp_f32_e32 v98, v98
	v_exp_f32_e32 v99, v99
	v_exp_f32_e32 v102, v102
	v_exp_f32_e32 v104, v104
	v_exp_f32_e32 v105, v105
	v_exp_f32_e32 v108, v108
	v_exp_f32_e32 v109, v109
	v_exp_f32_e32 v106, v106
	v_exp_f32_e32 v107, v107
	v_exp_f32_e32 v110, v110
	v_exp_f32_e32 v111, v111
	s_waitcnt lgkmcnt(4)
	v_mfma_f32_32x32x64_f8f6f4 v[112:127], v[218:225], v[168:175], v[80:95]
	ds_read_b128 v[218:221], v199 offset:8192
	ds_read_b128 v[222:225], v200 offset:8192
	ds_read_b128 v[226:229], v199 offset:10240
	ds_read_b128 v[230:233], v200 offset:10240
	s_waitcnt lgkmcnt(6)
	v_mfma_f32_32x32x64_f8f6f4 v[128:143], v[236:243], v[176:183], v[128:143]
	s_waitcnt lgkmcnt(4)
	v_mfma_f32_32x32x64_f8f6f4 v[112:127], v[244:251], v[176:183], v[112:127]
	s_mul_i32 s98, s1, 0x5000
	v_add_u32_e32 v253, s98, v193
	v_add_u32_e32 v254, s98, v194
	ds_read_b128 v[240:243], v254 offset:12288
	ds_read_b128 v[236:239], v253 offset:12288
	ds_read_b128 v[244:247], v253 offset:14336
	ds_read_b128 v[248:251], v254 offset:14336
	s_waitcnt lgkmcnt(6)
	v_mfma_f32_32x32x64_f8f6f4 v[128:143], v[218:225], v[160:167], v[128:143]
	v_exp_f32_e32 v218, v100
	v_exp_f32_e32 v219, v101
	v_exp_f32_e32 v220, v103
	s_nop 0
	v_cvt_pk_fp8_f32 v100, v217, v97
	v_cvt_pk_fp8_f32 v101, v218, v219
	v_cvt_pk_fp8_f32 v100, v98, v99 op_sel:[0,0,1]
	v_cvt_pk_fp8_f32 v101, v102, v220 op_sel:[0,0,1]
	s_waitcnt lgkmcnt(4)
	v_mfma_f32_32x32x64_f8f6f4 v[112:127], v[226:233], v[160:167], v[112:127]
	v_cvt_pk_fp8_f32 v96, v215, v216
	v_cvt_pk_fp8_f32 v97, v211, v212
	v_cvt_pk_fp8_f32 v98, v207, v208
	v_cvt_pk_fp8_f32 v102, v104, v105
	v_cvt_pk_fp8_f32 v99, v203, v204
	v_cvt_pk_fp8_f32 v103, v108, v109
	v_cvt_pk_fp8_f32 v96, v213, v214 op_sel:[0,0,1]
	v_cvt_pk_fp8_f32 v97, v209, v210 op_sel:[0,0,1]
	v_cvt_pk_fp8_f32 v98, v205, v206 op_sel:[0,0,1]
	v_cvt_pk_fp8_f32 v102, v106, v107 op_sel:[0,0,1]
	v_cvt_pk_fp8_f32 v99, v201, v202 op_sel:[0,0,1]
	v_cvt_pk_fp8_f32 v103, v110, v111 op_sel:[0,0,1]
	s_mul_i32 s46, s1, 0x5000
	s_add_i32 s46, s46, 0
	v_add_u32_e32 v202, s46, v194
	v_add_u32_e32 v201, s46, v193
	ds_read_b128 v[108:111], v202 offset:16384
	ds_read_b128 v[104:107], v201 offset:16384
	v_mfma_f32_32x32x64_f8f6f4 v[64:79], v[96:103], v[152:159], v[64:79]
	s_sub_i32 s46, s39, 64
	s_cmp_le_i32 s46, s0
	s_waitcnt lgkmcnt(4)
	v_mfma_f32_32x32x64_f8f6f4 v[48:63], v[96:103], v[236:243], v[48:63]
	ds_read_b128 v[236:239], v201 offset:18432
	ds_read_b128 v[240:243], v202 offset:18432
	s_waitcnt lgkmcnt(4)
	v_mfma_f32_32x32x64_f8f6f4 v[32:47], v[96:103], v[244:251], v[32:47]
	s_waitcnt lgkmcnt(2)
	v_mfma_f32_32x32x64_f8f6f4 v[16:31], v[96:103], v[104:111], v[16:31]
	s_waitcnt lgkmcnt(0)
	v_mfma_f32_32x32x64_f8f6f4 v[0:15], v[96:103], v[236:243], v[0:15]
	s_cbranch_scc1 .LBB0_669
	v_add_u32_e32 v96, 0x4000007b, v196
	v_cmp_gt_u32_e32 vcc, 2.0, v96
	v_add_u32_e32 v96, 0x5b, v196
	s_nop 0
	v_cndmask_b32_e32 v128, v187, v128, vcc
	v_cmp_lt_u32_e32 vcc, s3, v96
	v_add_u32_e32 v96, 0x7a, v196
	s_nop 0
	v_cndmask_b32_e32 v112, v187, v112, vcc
	v_cmp_lt_u32_e32 vcc, s3, v96
	v_add_u32_e32 v96, 0x5a, v196
	s_nop 0
	v_cndmask_b32_e32 v129, v187, v129, vcc
	v_cmp_lt_u32_e32 vcc, s3, v96
	v_add_u32_e32 v96, 0x79, v196
	s_nop 0
	v_cndmask_b32_e32 v113, v187, v113, vcc
	v_cmp_lt_u32_e32 vcc, s3, v96
	v_add_u32_e32 v96, 0x59, v196
	s_nop 0
	v_cndmask_b32_e32 v130, v187, v130, vcc
	v_cmp_lt_u32_e32 vcc, s3, v96
	v_add_u32_e32 v96, 0x78, v196
	s_nop 0
	v_cndmask_b32_e32 v114, v187, v114, vcc
	v_cmp_lt_u32_e32 vcc, s3, v96
	v_add_u32_e32 v96, 0x58, v196
	s_nop 0
	v_cndmask_b32_e32 v131, v187, v131, vcc
	v_cmp_lt_u32_e32 vcc, s3, v96
	v_add_u32_e32 v96, 0x73, v196
	s_nop 0
	v_cndmask_b32_e32 v115, v187, v115, vcc
	v_cmp_lt_u32_e32 vcc, s3, v96
	v_add_u32_e32 v96, 0x53, v196
	s_nop 0
	v_cndmask_b32_e32 v132, v187, v132, vcc
	v_cmp_lt_u32_e32 vcc, s3, v96
	v_add_u32_e32 v96, 0x72, v196
	s_nop 0
	v_cndmask_b32_e32 v116, v187, v116, vcc
	v_cmp_lt_u32_e32 vcc, s3, v96
	v_add_u32_e32 v96, 0x52, v196
	s_nop 0
	v_cndmask_b32_e32 v133, v187, v133, vcc
	v_cmp_lt_u32_e32 vcc, s3, v96
	v_add_u32_e32 v96, 0x71, v196
	s_nop 0
	v_cndmask_b32_e32 v117, v187, v117, vcc
	v_cmp_lt_u32_e32 vcc, s3, v96
	v_add_u32_e32 v96, 0x51, v196
	s_nop 0
	v_cndmask_b32_e32 v134, v187, v134, vcc
	v_cmp_lt_u32_e32 vcc, s3, v96
	v_add_u32_e32 v96, 0x70, v196
	s_nop 0
	v_cndmask_b32_e32 v118, v187, v118, vcc
	v_cmp_lt_u32_e32 vcc, s3, v96
	v_add_u32_e32 v96, 0x50, v196
	s_nop 0
	v_cndmask_b32_e32 v135, v187, v135, vcc
	v_cmp_lt_u32_e32 vcc, s3, v96
	v_add_u32_e32 v96, 0x6b, v196
	s_nop 0
	v_cndmask_b32_e32 v119, v187, v119, vcc
	v_cmp_lt_u32_e32 vcc, s3, v96
	v_add_u32_e32 v96, 0x4b, v196
	s_nop 0
	v_cndmask_b32_e32 v136, v187, v136, vcc
	v_cmp_lt_u32_e32 vcc, s3, v96
	v_add_u32_e32 v96, 0x6a, v196
	s_nop 0
	v_cndmask_b32_e32 v120, v187, v120, vcc
	v_cmp_lt_u32_e32 vcc, s3, v96
	v_add_u32_e32 v96, 0x4a, v196
	s_nop 0
	v_cndmask_b32_e32 v137, v187, v137, vcc
	v_cmp_lt_u32_e32 vcc, s3, v96
	v_add_u32_e32 v96, 0x69, v196
	s_nop 0
	v_cndmask_b32_e32 v121, v187, v121, vcc
	v_cmp_lt_u32_e32 vcc, s3, v96
	v_add_u32_e32 v96, 0x49, v196
	s_nop 0
	v_cndmask_b32_e32 v138, v187, v138, vcc
	v_cmp_lt_u32_e32 vcc, s3, v96
	v_add_u32_e32 v96, 0x68, v196
	s_nop 0
	v_cndmask_b32_e32 v122, v187, v122, vcc
	v_cmp_lt_u32_e32 vcc, s3, v96
	v_add_u32_e32 v96, 0x48, v196
	s_nop 0
	v_cndmask_b32_e32 v139, v187, v139, vcc
	v_cmp_lt_u32_e32 vcc, s3, v96
	v_add_u32_e32 v96, 0x63, v196
	s_nop 0
	v_cndmask_b32_e32 v123, v187, v123, vcc
	v_cmp_lt_u32_e32 vcc, s3, v96
	v_add_u32_e32 v96, 0x43, v196
	s_nop 0
	v_cndmask_b32_e32 v140, v187, v140, vcc
	v_cmp_lt_u32_e32 vcc, s3, v96
	v_add_u32_e32 v96, 0x62, v196
	s_nop 0
	v_cndmask_b32_e32 v124, v187, v124, vcc
	v_cmp_lt_u32_e32 vcc, s3, v96
	v_add_u32_e32 v96, 0x42, v196
	s_nop 0
	v_cndmask_b32_e32 v141, v187, v141, vcc
	v_cmp_lt_u32_e32 vcc, s3, v96
	v_add_u32_e32 v96, 0x61, v196
	s_nop 0
	v_cndmask_b32_e32 v125, v187, v125, vcc
	v_cmp_lt_u32_e32 vcc, s3, v96
	v_add_u32_e32 v96, 0x41, v196
	s_nop 0
	v_cndmask_b32_e32 v142, v187, v142, vcc
	v_cmp_lt_u32_e32 vcc, s3, v96
	v_add_u32_e32 v96, 0x60, v196
	s_nop 0
	v_cndmask_b32_e32 v126, v187, v126, vcc
	v_cmp_lt_u32_e32 vcc, s3, v96
	v_add_u32_e32 v96, 64, v196
	s_nop 0
	v_cndmask_b32_e32 v143, v187, v143, vcc
	v_cmp_lt_u32_e32 vcc, s3, v96
	s_nop 1
	v_cndmask_b32_e32 v127, v187, v127, vcc

; __device__ __forceinline__ unsigned cvt_pk4_fp8(float a, float b, float c, float d) { int w; asm("" : "=v"(w));     w = __builtin_amdgcn_cvt_pk_fp8_f32(a, b, w, false); w = __builtin_amdgcn_cvt_pk_fp8_f32(c, d, w, true); return (unsigned)w; }
; __device__ __forceinline__ void finishSM(f32x16& p0, f32x16& p1, i32x8& pa) {
;     for (int r = 0; r < 16; ++r) p1[r] = __builtin_amdgcn_exp2f(p1[r]);
; #pragma unroll
;     for (int v = 0; v < 4; ++v) { pa[v] = (int)cvt_pk4_fp8(p0[4 * v], p0[4 * v + 1], p0[4 * v + 2], p0[4 * v + 3]); pa[4 + v] = (int)cvt_pk4_fp8(p1[4 * v], p1[4 * v + 1], p1[4 * v + 2], p1[4 * v + 3]); }
; }
; __device__ __forceinline__ void qkt(f32x16& p0, f32x16& p1, const char* stg, int ka, const i32x8* qf, const f32x16& minit) {
;     p0 = minit; p1 = minit;
; #pragma unroll
;     for (int s = 0; s < 3; ++s) { const char* a = stg + SOFF_K + s * 4096 + ka; const char* b = stg + SOFF_K + s * 4096 + (ka ^ 16);
;         const i32x4 a0 = *reinterpret_cast<const i32x4*>(a), a1 = *reinterpret_cast<const i32x4*>(b);
;         const i32x4 c0 = *reinterpret_cast<const i32x4*>(a + 2048), c1 = *reinterpret_cast<const i32x4*>(b + 2048);
;         p0 = __builtin_amdgcn_mfma_scale_f32_32x32x64_f8f6f4(__builtin_shufflevector(a0, a1, 0, 1, 2, 3, 4, 5, 6, 7), qf[s], p0, 0, 0, 0, 0, 0, 0);
;         p1 = __builtin_amdgcn_mfma_scale_f32_32x32x64_f8f6f4(__builtin_shufflevector(c0, c1, 0, 1, 2, 3, 4, 5, 6, 7), qf[s], p1, 0, 0, 0, 0, 0, 0); }
; }
; __device__ __forceinline__ void v_read(i32x8 (&vf)[4], const char* stg, int ka) {
; #pragma unroll
;     for (int d0 = 0; d0 < 4; ++d0) { const i32x4 a0 = *reinterpret_cast<const i32x4*>(stg + SOFF_V + d0 * 2048 + ka), a1 = *reinterpret_cast<const i32x4*>(stg + SOFF_V + d0 * 2048 + (ka ^ 16));
;         vf[d0] = __builtin_shufflevector(a0, a1, 0, 1, 2, 3, 4, 5, 6, 7); }
; }
; __device__ __forceinline__ void pv_mma(f32x16* o, f32x16& ol, const i32x8 (&vf)[4], const i32x8 ones, const i32x8 pa) {
; #pragma unroll
;     for (int d0 = 0; d0 < 4; ++d0) o[d0] = __builtin_amdgcn_mfma_scale_f32_32x32x64_f8f6f4(pa, vf[d0], o[d0], 0, 0, 0, 0, 0, 0);
;     ol = __builtin_amdgcn_mfma_scale_f32_32x32x64_f8f6f4(pa, ones, ol, 0, 0, 0, 0, 0, 0);
; }
.LBB0_674:
	s_cmp_gt_i32 s1, 3
	s_cselect_b32 s46, -4, 2
	s_add_i32 s1, s46, s1
	v_exp_f32_e32 v201, v128
	v_exp_f32_e32 v218, v129
	v_exp_f32_e32 v219, v130
	v_exp_f32_e32 v220, v131
	v_exp_f32_e32 v221, v132
	v_exp_f32_e32 v222, v133
	v_exp_f32_e32 v223, v134
	v_exp_f32_e32 v224, v135
	v_exp_f32_e32 v225, v136
	v_exp_f32_e32 v226, v137
	v_exp_f32_e32 v227, v138
	v_exp_f32_e32 v228, v139
	v_exp_f32_e32 v229, v140
	v_exp_f32_e32 v230, v141
	v_exp_f32_e32 v231, v142
	v_exp_f32_e32 v232, v143
	s_mul_i32 s92, s1, 0x5000
	s_add_i32 s46, s92, 0
	v_add_u32_e32 v233, s46, v193
	v_add_u32_e32 v234, s46, v194
	ds_read_b128 v[202:205], v233
	ds_read_b128 v[206:209], v234
	ds_read_b128 v[210:213], v233 offset:2048
	ds_read_b128 v[214:217], v234 offset:2048
	ds_read_b128 v[236:239], v233 offset:4096
	ds_read_b128 v[240:243], v234 offset:4096
	ds_read_b128 v[244:247], v233 offset:6144
	ds_read_b128 v[248:251], v234 offset:6144
	v_exp_f32_e32 v113, v113
	s_waitcnt lgkmcnt(6)
	v_mfma_f32_32x32x64_f8f6f4 v[128:143], v[202:209], v[168:175], v[96:111]
	v_exp_f32_e32 v114, v114
	v_exp_f32_e32 v115, v115
	v_exp_f32_e32 v118, v118
	v_exp_f32_e32 v120, v120
	v_exp_f32_e32 v121, v121
	v_exp_f32_e32 v124, v124
	v_exp_f32_e32 v125, v125
	v_exp_f32_e32 v122, v122
	v_exp_f32_e32 v123, v123
	v_exp_f32_e32 v126, v126
	v_exp_f32_e32 v127, v127
	s_waitcnt lgkmcnt(4)
	v_mfma_f32_32x32x64_f8f6f4 v[96:111], v[210:217], v[168:175], v[96:111]
	ds_read_b128 v[202:205], v233 offset:8192
	ds_read_b128 v[206:209], v234 offset:8192
	ds_read_b128 v[210:213], v233 offset:10240
	ds_read_b128 v[214:217], v234 offset:10240
	s_waitcnt lgkmcnt(6)
	v_mfma_f32_32x32x64_f8f6f4 v[128:143], v[236:243], v[176:183], v[128:143]
	s_waitcnt lgkmcnt(4)
	v_mfma_f32_32x32x64_f8f6f4 v[96:111], v[244:251], v[176:183], v[96:111]
	ds_read_b128 v[240:243], v200 offset:12288
	ds_read_b128 v[236:239], v199 offset:12288
	ds_read_b128 v[244:247], v199 offset:14336
	ds_read_b128 v[248:251], v200 offset:14336
	s_waitcnt lgkmcnt(6)
	v_mfma_f32_32x32x64_f8f6f4 v[128:143], v[202:209], v[160:167], v[128:143]
	v_exp_f32_e32 v202, v112
	v_exp_f32_e32 v203, v116
	v_exp_f32_e32 v204, v117
	v_exp_f32_e32 v205, v119
	s_nop 0
	v_cvt_pk_fp8_f32 v116, v202, v113
	v_cvt_pk_fp8_f32 v117, v203, v204
	v_cvt_pk_fp8_f32 v116, v114, v115 op_sel:[0,0,1]
	v_cvt_pk_fp8_f32 v117, v118, v205 op_sel:[0,0,1]
	s_waitcnt lgkmcnt(4)
	v_mfma_f32_32x32x64_f8f6f4 v[96:111], v[210:217], v[160:167], v[96:111]
	v_cvt_pk_fp8_f32 v112, v201, v218
	v_cvt_pk_fp8_f32 v113, v221, v222
	v_cvt_pk_fp8_f32 v114, v225, v226
	v_cvt_pk_fp8_f32 v118, v120, v121
	v_cvt_pk_fp8_f32 v115, v229, v230
	v_cvt_pk_fp8_f32 v119, v124, v125
	v_cvt_pk_fp8_f32 v112, v219, v220 op_sel:[0,0,1]
	v_cvt_pk_fp8_f32 v113, v223, v224 op_sel:[0,0,1]
	v_cvt_pk_fp8_f32 v114, v227, v228 op_sel:[0,0,1]
	v_cvt_pk_fp8_f32 v118, v122, v123 op_sel:[0,0,1]
	v_cvt_pk_fp8_f32 v115, v231, v232 op_sel:[0,0,1]
	v_cvt_pk_fp8_f32 v119, v126, v127 op_sel:[0,0,1]
	ds_read_b128 v[124:127], v200 offset:16384
	ds_read_b128 v[120:123], v199 offset:16384
	v_mfma_f32_32x32x64_f8f6f4 v[64:79], v[112:119], v[152:159], v[64:79]
	s_cmp_le_i32 s39, s0
	s_waitcnt lgkmcnt(4)
	v_mfma_f32_32x32x64_f8f6f4 v[48:63], v[112:119], v[236:243], v[48:63]
	ds_read_b128 v[236:239], v199 offset:18432
	ds_read_b128 v[240:243], v200 offset:18432
	s_waitcnt lgkmcnt(4)
	v_mfma_f32_32x32x64_f8f6f4 v[32:47], v[112:119], v[244:251], v[32:47]
	s_waitcnt lgkmcnt(2)
	v_mfma_f32_32x32x64_f8f6f4 v[16:31], v[112:119], v[120:127], v[16:31]
	s_waitcnt lgkmcnt(0)
	v_mfma_f32_32x32x64_f8f6f4 v[0:15], v[112:119], v[236:243], v[0:15]
	s_cbranch_scc1 .LBB0_676
; __device__ __forceinline__ void mask_tile(f32x16& p0, f32x16& p1, int dq, unsigned W) {
;     const float NEG = -__builtin_inff();
; #pragma unroll
;     for (int r = 0; r < 16; ++r) {
;         const int c = (r & 3) + 8 * (r >> 2);
;         if ((unsigned)(dq - c) >= W) p0[r] = NEG;
;         if ((unsigned)(dq - c - 32) >= W) p1[r] = NEG;
;     }
; }
	v_add_u32_e32 v112, 0x4000003b, v196
	v_cmp_gt_u32_e32 vcc, 2.0, v112
	v_add_u32_e32 v112, 27, v196
	s_nop 0
	v_cndmask_b32_e32 v128, v187, v128, vcc
	v_cmp_lt_u32_e32 vcc, s3, v112
	v_add_u32_e32 v112, 58, v196
	s_nop 0
	v_cndmask_b32_e32 v96, v187, v96, vcc
	v_cmp_lt_u32_e32 vcc, s3, v112
	v_add_u32_e32 v112, 26, v196
	s_nop 0
	v_cndmask_b32_e32 v129, v187, v129, vcc
	v_cmp_lt_u32_e32 vcc, s3, v112
	v_add_u32_e32 v112, 57, v196
	s_nop 0
	v_cndmask_b32_e32 v97, v187, v97, vcc
	v_cmp_lt_u32_e32 vcc, s3, v112
	v_add_u32_e32 v112, 25, v196
	s_nop 0
	v_cndmask_b32_e32 v130, v187, v130, vcc
	v_cmp_lt_u32_e32 vcc, s3, v112
	v_add_u32_e32 v112, 56, v196
	s_nop 0
	v_cndmask_b32_e32 v98, v187, v98, vcc
	v_cmp_lt_u32_e32 vcc, s3, v112
	v_add_u32_e32 v112, 24, v196
	s_nop 0
	v_cndmask_b32_e32 v131, v187, v131, vcc
	v_cmp_lt_u32_e32 vcc, s3, v112
	v_add_u32_e32 v112, 51, v196
	s_nop 0
	v_cndmask_b32_e32 v99, v187, v99, vcc
	v_cmp_lt_u32_e32 vcc, s3, v112
	v_add_u32_e32 v112, 19, v196
	s_nop 0
	v_cndmask_b32_e32 v132, v187, v132, vcc
	v_cmp_lt_u32_e32 vcc, s3, v112
	v_add_u32_e32 v112, 50, v196
	s_nop 0
	v_cndmask_b32_e32 v100, v187, v100, vcc
	v_cmp_lt_u32_e32 vcc, s3, v112
	v_add_u32_e32 v112, 18, v196
	s_nop 0
	v_cndmask_b32_e32 v133, v187, v133, vcc
	v_cmp_lt_u32_e32 vcc, s3, v112
	v_add_u32_e32 v112, 49, v196
	s_nop 0
	v_cndmask_b32_e32 v101, v187, v101, vcc
	v_cmp_lt_u32_e32 vcc, s3, v112
	v_add_u32_e32 v112, 17, v196
	s_nop 0
	v_cndmask_b32_e32 v134, v187, v134, vcc
	v_cmp_lt_u32_e32 vcc, s3, v112
	v_add_u32_e32 v112, 48, v196
	s_nop 0
	v_cndmask_b32_e32 v102, v187, v102, vcc
	v_cmp_lt_u32_e32 vcc, s3, v112
	v_add_u32_e32 v112, 16, v196
	s_nop 0
	v_cndmask_b32_e32 v135, v187, v135, vcc
	v_cmp_lt_u32_e32 vcc, s3, v112
	v_add_u32_e32 v112, 43, v196
	s_nop 0
	v_cndmask_b32_e32 v103, v187, v103, vcc
	v_cmp_lt_u32_e32 vcc, s3, v112
	v_add_u32_e32 v112, 11, v196
	s_nop 0
	v_cndmask_b32_e32 v136, v187, v136, vcc
	v_cmp_lt_u32_e32 vcc, s3, v112
	v_add_u32_e32 v112, 42, v196
	s_nop 0
	v_cndmask_b32_e32 v104, v187, v104, vcc
	v_cmp_lt_u32_e32 vcc, s3, v112
	v_add_u32_e32 v112, 10, v196
	s_nop 0
	v_cndmask_b32_e32 v137, v187, v137, vcc
	v_cmp_lt_u32_e32 vcc, s3, v112
	v_add_u32_e32 v112, 41, v196
	s_nop 0
	v_cndmask_b32_e32 v105, v187, v105, vcc
	v_cmp_lt_u32_e32 vcc, s3, v112
	v_add_u32_e32 v112, 9, v196
	s_nop 0
	v_cndmask_b32_e32 v138, v187, v138, vcc
	v_cmp_lt_u32_e32 vcc, s3, v112
	v_add_u32_e32 v112, 40, v196
	s_nop 0
	v_cndmask_b32_e32 v106, v187, v106, vcc
	v_cmp_lt_u32_e32 vcc, s3, v112
	v_add_u32_e32 v112, 8, v196
	s_nop 0
	v_cndmask_b32_e32 v139, v187, v139, vcc
	v_cmp_lt_u32_e32 vcc, s3, v112
	v_add_u32_e32 v112, 35, v196
	s_nop 0
	v_cndmask_b32_e32 v107, v187, v107, vcc
	v_cmp_lt_u32_e32 vcc, s3, v112
	v_add_u32_e32 v112, 3, v196
	s_nop 0
	v_cndmask_b32_e32 v140, v187, v140, vcc
	v_cmp_lt_u32_e32 vcc, s3, v112
	v_add_u32_e32 v112, 34, v196
	s_nop 0
	v_cndmask_b32_e32 v108, v187, v108, vcc
	v_cmp_lt_u32_e32 vcc, s3, v112
	v_add_u32_e32 v112, 2, v196
	s_nop 0
	v_cndmask_b32_e32 v141, v187, v141, vcc
	v_cmp_lt_u32_e32 vcc, s3, v112
	v_add_u32_e32 v112, 33, v196
	s_nop 0
	v_cndmask_b32_e32 v109, v187, v109, vcc
	v_cmp_lt_u32_e32 vcc, s3, v112
	v_add_u32_e32 v112, 1, v196
	s_nop 0
	v_cndmask_b32_e32 v142, v187, v142, vcc
	v_cmp_lt_u32_e32 vcc, s3, v112
	v_add_u32_e32 v112, 32, v196
	s_nop 0
	v_cndmask_b32_e32 v110, v187, v110, vcc
	v_cmp_lt_u32_e32 vcc, s3, v112
	s_nop 1
	v_cndmask_b32_e32 v143, v187, v143, vcc
	v_cmp_lt_u32_e32 vcc, s3, v196
	s_nop 1
	v_cndmask_b32_e32 v111, v187, v111, vcc

; __device__ __forceinline__ void mask_tile(f32x16& p0, f32x16& p1, int dq, unsigned W) {
;     const float NEG = -__builtin_inff();
; #pragma unroll
;     for (int r = 0; r < 16; ++r) {
;         const int c = (r & 3) + 8 * (r >> 2);
;         if ((unsigned)(dq - c) >= W) p0[r] = NEG;
;         if ((unsigned)(dq - c - 32) >= W) p1[r] = NEG;
;     }
; }
; template <bool FIRST>
; __device__ __forceinline__ bool partialSM(f32x16& p0, f32x16& p1, float& M, f32x16& minit, float& alpha) {
;     float tmax = p0[0]; for (int r = 1; r < 16; ++r) tmax = fmaxf(tmax, p0[r]); for (int r = 0; r < 16; ++r) tmax = fmaxf(tmax, p1[r]);
;     { auto rr = __builtin_amdgcn_permlane32_swap(__float_as_uint(tmax), __float_as_uint(tmax), false, false);
;       tmax = fmaxf(__uint_as_float(rr[0]), __uint_as_float(rr[1])); }
;     const float d0 = tmax - PLOG2;
;     const bool moved = FIRST || !__all(d0 <= THR * 1.4426950408889634f);
;     if (__builtin_expect(moved, FIRST)) {
;         const float d = FIRST ? d0 : fmaxf(d0, 0.f);
;         alpha = __builtin_amdgcn_exp2f(-d); M += d;
;         for (int r = 0; r < 16; ++r) { p0[r] -= d; p1[r] -= d; }
;         const float mi = PLOG2 - M;
;         for (int r = 0; r < 16; ++r) minit[r] = mi;
;     } else alpha = 1.f;
;     for (int r = 0; r < 16; ++r) p0[r] = __builtin_amdgcn_exp2f(p0[r]);
;     return moved;
; }
; __device__ __forceinline__ void finishSM(f32x16& p0, f32x16& p1, i32x8& pa) {
;     for (int r = 0; r < 16; ++r) p1[r] = __builtin_amdgcn_exp2f(p1[r]);
; #pragma unroll
;     for (int v = 0; v < 4; ++v) { pa[v] = (int)cvt_pk4_fp8(p0[4 * v], p0[4 * v + 1], p0[4 * v + 2], p0[4 * v + 3]); pa[4 + v] = (int)cvt_pk4_fp8(p1[4 * v], p1[4 * v + 1], p1[4 * v + 2], p1[4 * v + 3]); }
; }
; __device__ __forceinline__ void qkt(f32x16& p0, f32x16& p1, const char* stg, int ka, const i32x8* qf, const f32x16& minit) {
;     p0 = minit; p1 = minit;
; #pragma unroll
;     for (int s = 0; s < 3; ++s) { const char* a = stg + SOFF_K + s * 4096 + ka; const char* b = stg + SOFF_K + s * 4096 + (ka ^ 16);
;         const i32x4 a0 = *reinterpret_cast<const i32x4*>(a), a1 = *reinterpret_cast<const i32x4*>(b);
;         const i32x4 c0 = *reinterpret_cast<const i32x4*>(a + 2048), c1 = *reinterpret_cast<const i32x4*>(b + 2048);
.LBB0_729:
	s_cmp_gt_i32 s0, 4
	s_cselect_b32 s36, -5, 1
	s_add_i32 s36, s36, s0
	s_mulk_i32 s36, 0x5000
	s_add_i32 s36, s36, 0
	v_add_u32_e32 v199, s36, v192
	v_add_u32_e32 v200, s36, v193
	ds_read_b128 v[112:115], v199
	ds_read_b128 v[116:119], v200
	ds_read_b128 v[220:223], v199 offset:2048
	ds_read_b128 v[224:227], v200 offset:2048
	ds_read_b128 v[236:239], v199 offset:4096
	ds_read_b128 v[240:243], v200 offset:4096
	ds_read_b128 v[244:247], v199 offset:6144
	ds_read_b128 v[248:251], v200 offset:6144
	v_exp_f32_e32 v201, v96
	s_waitcnt lgkmcnt(6)
	v_mfma_f32_32x32x64_f8f6f4 v[128:143], v[112:119], v[168:175], v[80:95]
	v_exp_f32_e32 v97, v97
	v_exp_f32_e32 v202, v100
	v_exp_f32_e32 v219, v101
	v_exp_f32_e32 v98, v98
	v_exp_f32_e32 v99, v99
	v_exp_f32_e32 v102, v102
	v_exp_f32_e32 v104, v104
	v_exp_f32_e32 v105, v105
	v_exp_f32_e32 v108, v108
	v_exp_f32_e32 v109, v109
	v_exp_f32_e32 v106, v106
	v_exp_f32_e32 v107, v107
	v_exp_f32_e32 v110, v110
	v_exp_f32_e32 v111, v111
	s_waitcnt lgkmcnt(4)
	v_mfma_f32_32x32x64_f8f6f4 v[112:127], v[220:227], v[168:175], v[80:95]
	ds_read_b128 v[220:223], v199 offset:8192
	ds_read_b128 v[224:227], v200 offset:8192
	ds_read_b128 v[228:231], v199 offset:10240
	ds_read_b128 v[232:235], v200 offset:10240
	s_waitcnt lgkmcnt(6)
	v_mfma_f32_32x32x64_f8f6f4 v[128:143], v[236:243], v[176:183], v[128:143]
	s_waitcnt lgkmcnt(4)
	v_mfma_f32_32x32x64_f8f6f4 v[112:127], v[244:251], v[176:183], v[112:127]
	s_mul_i32 s98, s0, 0x5000
	v_add_u32_e32 v253, s98, v192
	v_add_u32_e32 v254, s98, v193
	ds_read_b128 v[240:243], v254 offset:12288
	ds_read_b128 v[236:239], v253 offset:12288
	ds_read_b128 v[244:247], v253 offset:14336
	ds_read_b128 v[248:251], v254 offset:14336
	s_waitcnt lgkmcnt(6)
	v_mfma_f32_32x32x64_f8f6f4 v[128:143], v[220:227], v[160:167], v[128:143]
	v_exp_f32_e32 v220, v103
	s_nop 0
	v_cvt_pk_fp8_f32 v100, v201, v97
	v_cvt_pk_fp8_f32 v101, v202, v219
	v_cvt_pk_fp8_f32 v100, v98, v99 op_sel:[0,0,1]
	v_cvt_pk_fp8_f32 v101, v102, v220 op_sel:[0,0,1]
	v_cvt_pk_fp8_f32 v96, v217, v218
	s_waitcnt lgkmcnt(4)
	v_mfma_f32_32x32x64_f8f6f4 v[112:127], v[228:235], v[160:167], v[112:127]
	v_cvt_pk_fp8_f32 v97, v213, v214
	v_cvt_pk_fp8_f32 v98, v209, v210
	v_cvt_pk_fp8_f32 v102, v104, v105
	v_cvt_pk_fp8_f32 v99, v205, v206
	v_cvt_pk_fp8_f32 v103, v108, v109
	v_cvt_pk_fp8_f32 v96, v215, v216 op_sel:[0,0,1]
	v_cvt_pk_fp8_f32 v97, v211, v212 op_sel:[0,0,1]
	v_cvt_pk_fp8_f32 v98, v207, v208 op_sel:[0,0,1]
	v_cvt_pk_fp8_f32 v102, v106, v107 op_sel:[0,0,1]
	v_cvt_pk_fp8_f32 v99, v203, v204 op_sel:[0,0,1]
	v_cvt_pk_fp8_f32 v103, v110, v111 op_sel:[0,0,1]
	s_mul_i32 s36, s0, 0x5000
	s_add_i32 s36, s36, 0
	v_add_u32_e32 v202, s36, v193
	v_add_u32_e32 v201, s36, v192
	ds_read_b128 v[108:111], v202 offset:16384
	ds_read_b128 v[104:107], v201 offset:16384
	v_mfma_f32_32x32x64_f8f6f4 v[64:79], v[96:103], v[152:159], v[64:79]
	s_sub_i32 s36, s1, 64
	s_cmp_le_u32 s36, s39
	s_waitcnt lgkmcnt(4)
	v_mfma_f32_32x32x64_f8f6f4 v[48:63], v[96:103], v[236:243], v[48:63]
	ds_read_b128 v[236:239], v201 offset:18432
	ds_read_b128 v[240:243], v202 offset:18432
	s_waitcnt lgkmcnt(4)
	v_mfma_f32_32x32x64_f8f6f4 v[0:15], v[96:103], v[244:251], v[0:15]
	s_waitcnt lgkmcnt(2)
	v_mfma_f32_32x32x64_f8f6f4 v[32:47], v[96:103], v[104:111], v[32:47]
	s_waitcnt lgkmcnt(0)
	v_mfma_f32_32x32x64_f8f6f4 v[16:31], v[96:103], v[236:243], v[16:31]
	s_cbranch_scc1 .LBB0_731
	v_add_u32_e32 v96, 0x4000007b, v198
	v_cmp_gt_u32_e32 vcc, 2.0, v96
	v_add_u32_e32 v96, 0x5b, v198
	s_nop 0
	v_cndmask_b32_e32 v128, v187, v128, vcc
	v_cmp_lt_u32_e32 vcc, s41, v96
	v_add_u32_e32 v96, 0x7a, v198
	s_nop 0
	v_cndmask_b32_e32 v112, v187, v112, vcc
	v_cmp_lt_u32_e32 vcc, s41, v96
	v_add_u32_e32 v96, 0x5a, v198
	s_nop 0
	v_cndmask_b32_e32 v129, v187, v129, vcc
	v_cmp_lt_u32_e32 vcc, s41, v96
	v_add_u32_e32 v96, 0x79, v198
	s_nop 0
	v_cndmask_b32_e32 v113, v187, v113, vcc
	v_cmp_lt_u32_e32 vcc, s41, v96
	v_add_u32_e32 v96, 0x59, v198
	s_nop 0
	v_cndmask_b32_e32 v130, v187, v130, vcc
	v_cmp_lt_u32_e32 vcc, s41, v96
	v_add_u32_e32 v96, 0x78, v198
	s_nop 0
	v_cndmask_b32_e32 v114, v187, v114, vcc
	v_cmp_lt_u32_e32 vcc, s41, v96
	v_add_u32_e32 v96, 0x58, v198
	s_nop 0
	v_cndmask_b32_e32 v131, v187, v131, vcc
	v_cmp_lt_u32_e32 vcc, s41, v96
	v_add_u32_e32 v96, 0x73, v198
	s_nop 0
	v_cndmask_b32_e32 v115, v187, v115, vcc
	v_cmp_lt_u32_e32 vcc, s41, v96
	v_add_u32_e32 v96, 0x53, v198
	s_nop 0
	v_cndmask_b32_e32 v132, v187, v132, vcc
	v_cmp_lt_u32_e32 vcc, s41, v96
	v_add_u32_e32 v96, 0x72, v198
	s_nop 0
	v_cndmask_b32_e32 v116, v187, v116, vcc
	v_cmp_lt_u32_e32 vcc, s41, v96
	v_add_u32_e32 v96, 0x52, v198
	s_nop 0
	v_cndmask_b32_e32 v133, v187, v133, vcc
	v_cmp_lt_u32_e32 vcc, s41, v96
	v_add_u32_e32 v96, 0x71, v198
	s_nop 0
	v_cndmask_b32_e32 v117, v187, v117, vcc
	v_cmp_lt_u32_e32 vcc, s41, v96
	v_add_u32_e32 v96, 0x51, v198
	s_nop 0
	v_cndmask_b32_e32 v134, v187, v134, vcc
	v_cmp_lt_u32_e32 vcc, s41, v96
	v_add_u32_e32 v96, 0x70, v198
	s_nop 0
	v_cndmask_b32_e32 v118, v187, v118, vcc
	v_cmp_lt_u32_e32 vcc, s41, v96
	v_add_u32_e32 v96, 0x50, v198
	s_nop 0
	v_cndmask_b32_e32 v135, v187, v135, vcc
	v_cmp_lt_u32_e32 vcc, s41, v96
	v_add_u32_e32 v96, 0x6b, v198
	s_nop 0
	v_cndmask_b32_e32 v119, v187, v119, vcc
	v_cmp_lt_u32_e32 vcc, s41, v96
	v_add_u32_e32 v96, 0x4b, v198
	s_nop 0
	v_cndmask_b32_e32 v136, v187, v136, vcc
	v_cmp_lt_u32_e32 vcc, s41, v96
	v_add_u32_e32 v96, 0x6a, v198
	s_nop 0
	v_cndmask_b32_e32 v120, v187, v120, vcc
	v_cmp_lt_u32_e32 vcc, s41, v96
	v_add_u32_e32 v96, 0x4a, v198
	s_nop 0
	v_cndmask_b32_e32 v137, v187, v137, vcc
	v_cmp_lt_u32_e32 vcc, s41, v96
	v_add_u32_e32 v96, 0x69, v198
	s_nop 0
	v_cndmask_b32_e32 v121, v187, v121, vcc
	v_cmp_lt_u32_e32 vcc, s41, v96
	v_add_u32_e32 v96, 0x49, v198
	s_nop 0
	v_cndmask_b32_e32 v138, v187, v138, vcc
	v_cmp_lt_u32_e32 vcc, s41, v96
	v_add_u32_e32 v96, 0x68, v198
	s_nop 0
	v_cndmask_b32_e32 v122, v187, v122, vcc
	v_cmp_lt_u32_e32 vcc, s41, v96
	v_add_u32_e32 v96, 0x48, v198
	s_nop 0
	v_cndmask_b32_e32 v139, v187, v139, vcc
	v_cmp_lt_u32_e32 vcc, s41, v96
	v_add_u32_e32 v96, 0x63, v198
	s_nop 0
	v_cndmask_b32_e32 v123, v187, v123, vcc
	v_cmp_lt_u32_e32 vcc, s41, v96
	v_add_u32_e32 v96, 0x43, v198
	s_nop 0
	v_cndmask_b32_e32 v140, v187, v140, vcc
	v_cmp_lt_u32_e32 vcc, s41, v96
	v_add_u32_e32 v96, 0x62, v198
	s_nop 0
	v_cndmask_b32_e32 v124, v187, v124, vcc
	v_cmp_lt_u32_e32 vcc, s41, v96
	v_add_u32_e32 v96, 0x42, v198
	s_nop 0
	v_cndmask_b32_e32 v141, v187, v141, vcc
	v_cmp_lt_u32_e32 vcc, s41, v96
	v_add_u32_e32 v96, 0x61, v198
	s_nop 0
	v_cndmask_b32_e32 v125, v187, v125, vcc
	v_cmp_lt_u32_e32 vcc, s41, v96
	v_add_u32_e32 v96, 0x41, v198
	s_nop 0
	v_cndmask_b32_e32 v142, v187, v142, vcc
	v_cmp_lt_u32_e32 vcc, s41, v96
	v_add_u32_e32 v96, 0x60, v198
	s_nop 0
	v_cndmask_b32_e32 v126, v187, v126, vcc
	v_cmp_lt_u32_e32 vcc, s41, v96
	v_add_u32_e32 v96, 64, v198
	s_nop 0
	v_cndmask_b32_e32 v143, v187, v143, vcc
	v_cmp_lt_u32_e32 vcc, s41, v96
	s_nop 1
	v_cndmask_b32_e32 v127, v187, v127, vcc

; __device__ __forceinline__ unsigned cvt_pk4_fp8(float a, float b, float c, float d) { int w; asm("" : "=v"(w));     w = __builtin_amdgcn_cvt_pk_fp8_f32(a, b, w, false); w = __builtin_amdgcn_cvt_pk_fp8_f32(c, d, w, true); return (unsigned)w; }
; __device__ __forceinline__ void finishSM(f32x16& p0, f32x16& p1, i32x8& pa) {
;     for (int r = 0; r < 16; ++r) p1[r] = __builtin_amdgcn_exp2f(p1[r]);
; #pragma unroll
;     for (int v = 0; v < 4; ++v) { pa[v] = (int)cvt_pk4_fp8(p0[4 * v], p0[4 * v + 1], p0[4 * v + 2], p0[4 * v + 3]); pa[4 + v] = (int)cvt_pk4_fp8(p1[4 * v], p1[4 * v + 1], p1[4 * v + 2], p1[4 * v + 3]); }
; }
; __device__ __forceinline__ void qkt(f32x16& p0, f32x16& p1, const char* stg, int ka, const i32x8* qf, const f32x16& minit) {
;     p0 = minit; p1 = minit;
; #pragma unroll
;     for (int s = 0; s < 3; ++s) { const char* a = stg + SOFF_K + s * 4096 + ka; const char* b = stg + SOFF_K + s * 4096 + (ka ^ 16);
;         const i32x4 a0 = *reinterpret_cast<const i32x4*>(a), a1 = *reinterpret_cast<const i32x4*>(b);
;         const i32x4 c0 = *reinterpret_cast<const i32x4*>(a + 2048), c1 = *reinterpret_cast<const i32x4*>(b + 2048);
;         p0 = __builtin_amdgcn_mfma_scale_f32_32x32x64_f8f6f4(__builtin_shufflevector(a0, a1, 0, 1, 2, 3, 4, 5, 6, 7), qf[s], p0, 0, 0, 0, 0, 0, 0);
;         p1 = __builtin_amdgcn_mfma_scale_f32_32x32x64_f8f6f4(__builtin_shufflevector(c0, c1, 0, 1, 2, 3, 4, 5, 6, 7), qf[s], p1, 0, 0, 0, 0, 0, 0); }
; }
; __device__ __forceinline__ void v_read(i32x8 (&vf)[4], const char* stg, int ka) {
; #pragma unroll
;     for (int d0 = 0; d0 < 4; ++d0) { const i32x4 a0 = *reinterpret_cast<const i32x4*>(stg + SOFF_V + d0 * 2048 + ka), a1 = *reinterpret_cast<const i32x4*>(stg + SOFF_V + d0 * 2048 + (ka ^ 16));
;         vf[d0] = __builtin_shufflevector(a0, a1, 0, 1, 2, 3, 4, 5, 6, 7); }
; }
; __device__ __forceinline__ void pv_mma(f32x16* o, f32x16& ol, const i32x8 (&vf)[4], const i32x8 ones, const i32x8 pa) {
; #pragma unroll
;     for (int d0 = 0; d0 < 4; ++d0) o[d0] = __builtin_amdgcn_mfma_scale_f32_32x32x64_f8f6f4(pa, vf[d0], o[d0], 0, 0, 0, 0, 0, 0);
;     ol = __builtin_amdgcn_mfma_scale_f32_32x32x64_f8f6f4(pa, ones, ol, 0, 0, 0, 0, 0, 0);
; }
.LBB0_736:
	s_cmp_gt_i32 s0, 3
	s_cselect_b32 s36, -4, 2
	s_add_i32 s0, s36, s0
	v_exp_f32_e32 v203, v128
	v_exp_f32_e32 v220, v129
	v_exp_f32_e32 v221, v130
	v_exp_f32_e32 v222, v131
	v_exp_f32_e32 v223, v132
	v_exp_f32_e32 v224, v133
	v_exp_f32_e32 v225, v134
	v_exp_f32_e32 v226, v135
	v_exp_f32_e32 v227, v136
	v_exp_f32_e32 v228, v137
	v_exp_f32_e32 v229, v138
	v_exp_f32_e32 v230, v139
	v_exp_f32_e32 v231, v140
	v_exp_f32_e32 v232, v141
	v_exp_f32_e32 v233, v142
	v_exp_f32_e32 v234, v143
	s_mul_i32 s36, s0, 0x5000
	s_add_i32 s36, s36, 0
	v_add_u32_e32 v202, s36, v192
	v_add_u32_e32 v201, s36, v193
	ds_read_b128 v[204:207], v202
	ds_read_b128 v[208:211], v201
	ds_read_b128 v[212:215], v202 offset:2048
	ds_read_b128 v[216:219], v201 offset:2048
	ds_read_b128 v[236:239], v202 offset:4096
	ds_read_b128 v[240:243], v201 offset:4096
	ds_read_b128 v[244:247], v202 offset:6144
	ds_read_b128 v[248:251], v201 offset:6144
	v_exp_f32_e32 v113, v113
	s_waitcnt lgkmcnt(6)
	v_mfma_f32_32x32x64_f8f6f4 v[128:143], v[204:211], v[168:175], v[96:111]
	v_exp_f32_e32 v114, v114
	v_exp_f32_e32 v115, v115
	v_exp_f32_e32 v118, v118
	v_exp_f32_e32 v120, v120
	v_exp_f32_e32 v121, v121
	v_exp_f32_e32 v124, v124
	v_exp_f32_e32 v125, v125
	v_exp_f32_e32 v122, v122
	v_exp_f32_e32 v123, v123
	v_exp_f32_e32 v126, v126
	v_exp_f32_e32 v127, v127
	s_waitcnt lgkmcnt(4)
	v_mfma_f32_32x32x64_f8f6f4 v[96:111], v[212:219], v[168:175], v[96:111]
	ds_read_b128 v[204:207], v202 offset:8192
	ds_read_b128 v[208:211], v201 offset:8192
	ds_read_b128 v[212:215], v202 offset:10240
	ds_read_b128 v[216:219], v201 offset:10240
	s_waitcnt lgkmcnt(6)
	v_mfma_f32_32x32x64_f8f6f4 v[128:143], v[236:243], v[176:183], v[128:143]
	s_waitcnt lgkmcnt(4)
	v_mfma_f32_32x32x64_f8f6f4 v[96:111], v[244:251], v[176:183], v[96:111]
	ds_read_b128 v[240:243], v200 offset:12288
	ds_read_b128 v[236:239], v199 offset:12288
	ds_read_b128 v[244:247], v199 offset:14336
	ds_read_b128 v[248:251], v200 offset:14336
	s_waitcnt lgkmcnt(6)
	v_mfma_f32_32x32x64_f8f6f4 v[128:143], v[204:211], v[160:167], v[128:143]
	v_exp_f32_e32 v204, v112
	v_exp_f32_e32 v205, v116
	v_exp_f32_e32 v206, v117
	v_exp_f32_e32 v207, v119
	s_nop 0
	v_cvt_pk_fp8_f32 v116, v204, v113
	v_cvt_pk_fp8_f32 v117, v205, v206
	v_cvt_pk_fp8_f32 v116, v114, v115 op_sel:[0,0,1]
	v_cvt_pk_fp8_f32 v117, v118, v207 op_sel:[0,0,1]
	s_waitcnt lgkmcnt(4)
	v_mfma_f32_32x32x64_f8f6f4 v[96:111], v[212:219], v[160:167], v[96:111]
	v_cvt_pk_fp8_f32 v112, v203, v220
	v_cvt_pk_fp8_f32 v113, v223, v224
	v_cvt_pk_fp8_f32 v114, v227, v228
	v_cvt_pk_fp8_f32 v118, v120, v121
	v_cvt_pk_fp8_f32 v115, v231, v232
	v_cvt_pk_fp8_f32 v119, v124, v125
	v_cvt_pk_fp8_f32 v112, v221, v222 op_sel:[0,0,1]
	v_cvt_pk_fp8_f32 v113, v225, v226 op_sel:[0,0,1]
	v_cvt_pk_fp8_f32 v114, v229, v230 op_sel:[0,0,1]
	v_cvt_pk_fp8_f32 v118, v122, v123 op_sel:[0,0,1]
	v_cvt_pk_fp8_f32 v115, v233, v234 op_sel:[0,0,1]
	v_cvt_pk_fp8_f32 v119, v126, v127 op_sel:[0,0,1]
	ds_read_b128 v[124:127], v200 offset:16384
	ds_read_b128 v[120:123], v199 offset:16384
	v_mfma_f32_32x32x64_f8f6f4 v[64:79], v[112:119], v[152:159], v[64:79]
	s_cmp_le_u32 s1, s39
	s_waitcnt lgkmcnt(4)
	v_mfma_f32_32x32x64_f8f6f4 v[48:63], v[112:119], v[236:243], v[48:63]
	ds_read_b128 v[236:239], v199 offset:18432
	ds_read_b128 v[240:243], v200 offset:18432
	s_waitcnt lgkmcnt(4)
	v_mfma_f32_32x32x64_f8f6f4 v[0:15], v[112:119], v[244:251], v[0:15]
	s_waitcnt lgkmcnt(2)
	v_mfma_f32_32x32x64_f8f6f4 v[32:47], v[112:119], v[120:127], v[32:47]
	s_waitcnt lgkmcnt(0)
	v_mfma_f32_32x32x64_f8f6f4 v[16:31], v[112:119], v[236:243], v[16:31]
	s_cbranch_scc1 .LBB0_738
; __device__ __forceinline__ void mask_tile(f32x16& p0, f32x16& p1, int dq, unsigned W) {
;     const float NEG = -__builtin_inff();
; #pragma unroll
;     for (int r = 0; r < 16; ++r) {
;         const int c = (r & 3) + 8 * (r >> 2);
;         if ((unsigned)(dq - c) >= W) p0[r] = NEG;
;         if ((unsigned)(dq - c - 32) >= W) p1[r] = NEG;
;     }
; }
	v_add_u32_e32 v112, 0x4000003b, v198
	v_cmp_gt_u32_e32 vcc, 2.0, v112
	v_add_u32_e32 v112, 27, v198
	s_nop 0
	v_cndmask_b32_e32 v128, v187, v128, vcc
	v_cmp_lt_u32_e32 vcc, s41, v112
	v_add_u32_e32 v112, 58, v198
	s_nop 0
	v_cndmask_b32_e32 v96, v187, v96, vcc
	v_cmp_lt_u32_e32 vcc, s41, v112
	v_add_u32_e32 v112, 26, v198
	s_nop 0
	v_cndmask_b32_e32 v129, v187, v129, vcc
	v_cmp_lt_u32_e32 vcc, s41, v112
	v_add_u32_e32 v112, 57, v198
	s_nop 0
	v_cndmask_b32_e32 v97, v187, v97, vcc
	v_cmp_lt_u32_e32 vcc, s41, v112
	v_add_u32_e32 v112, 25, v198
	s_nop 0
	v_cndmask_b32_e32 v130, v187, v130, vcc
	v_cmp_lt_u32_e32 vcc, s41, v112
	v_add_u32_e32 v112, 56, v198
	s_nop 0
	v_cndmask_b32_e32 v98, v187, v98, vcc
	v_cmp_lt_u32_e32 vcc, s41, v112
	v_add_u32_e32 v112, 24, v198
	s_nop 0
	v_cndmask_b32_e32 v131, v187, v131, vcc
	v_cmp_lt_u32_e32 vcc, s41, v112
	v_add_u32_e32 v112, 51, v198
	s_nop 0
	v_cndmask_b32_e32 v99, v187, v99, vcc
	v_cmp_lt_u32_e32 vcc, s41, v112
	v_add_u32_e32 v112, 19, v198
	s_nop 0
	v_cndmask_b32_e32 v132, v187, v132, vcc
	v_cmp_lt_u32_e32 vcc, s41, v112
	v_add_u32_e32 v112, 50, v198
	s_nop 0
	v_cndmask_b32_e32 v100, v187, v100, vcc
	v_cmp_lt_u32_e32 vcc, s41, v112
	v_add_u32_e32 v112, 18, v198
	s_nop 0
	v_cndmask_b32_e32 v133, v187, v133, vcc
	v_cmp_lt_u32_e32 vcc, s41, v112
	v_add_u32_e32 v112, 49, v198
	s_nop 0
	v_cndmask_b32_e32 v101, v187, v101, vcc
	v_cmp_lt_u32_e32 vcc, s41, v112
	v_add_u32_e32 v112, 17, v198
	s_nop 0
	v_cndmask_b32_e32 v134, v187, v134, vcc
	v_cmp_lt_u32_e32 vcc, s41, v112
	v_add_u32_e32 v112, 48, v198
	s_nop 0
	v_cndmask_b32_e32 v102, v187, v102, vcc
	v_cmp_lt_u32_e32 vcc, s41, v112
	v_add_u32_e32 v112, 16, v198
	s_nop 0
	v_cndmask_b32_e32 v135, v187, v135, vcc
	v_cmp_lt_u32_e32 vcc, s41, v112
	v_add_u32_e32 v112, 43, v198
	s_nop 0
	v_cndmask_b32_e32 v103, v187, v103, vcc
	v_cmp_lt_u32_e32 vcc, s41, v112
	v_add_u32_e32 v112, 11, v198
	s_nop 0
	v_cndmask_b32_e32 v136, v187, v136, vcc
	v_cmp_lt_u32_e32 vcc, s41, v112
	v_add_u32_e32 v112, 42, v198
	s_nop 0
	v_cndmask_b32_e32 v104, v187, v104, vcc
	v_cmp_lt_u32_e32 vcc, s41, v112
	v_add_u32_e32 v112, 10, v198
	s_nop 0
	v_cndmask_b32_e32 v137, v187, v137, vcc
	v_cmp_lt_u32_e32 vcc, s41, v112
	v_add_u32_e32 v112, 41, v198
	s_nop 0
	v_cndmask_b32_e32 v105, v187, v105, vcc
	v_cmp_lt_u32_e32 vcc, s41, v112
	v_add_u32_e32 v112, 9, v198
	s_nop 0
	v_cndmask_b32_e32 v138, v187, v138, vcc
	v_cmp_lt_u32_e32 vcc, s41, v112
	v_add_u32_e32 v112, 40, v198
	s_nop 0
	v_cndmask_b32_e32 v106, v187, v106, vcc
	v_cmp_lt_u32_e32 vcc, s41, v112
	v_add_u32_e32 v112, 8, v198
	s_nop 0
	v_cndmask_b32_e32 v139, v187, v139, vcc
	v_cmp_lt_u32_e32 vcc, s41, v112
	v_add_u32_e32 v112, 35, v198
	s_nop 0
	v_cndmask_b32_e32 v107, v187, v107, vcc
	v_cmp_lt_u32_e32 vcc, s41, v112
	v_add_u32_e32 v112, 3, v198
	s_nop 0
	v_cndmask_b32_e32 v140, v187, v140, vcc
	v_cmp_lt_u32_e32 vcc, s41, v112
	v_add_u32_e32 v112, 34, v198
	s_nop 0
	v_cndmask_b32_e32 v108, v187, v108, vcc
	v_cmp_lt_u32_e32 vcc, s41, v112
	v_add_u32_e32 v112, 2, v198
	s_nop 0
	v_cndmask_b32_e32 v141, v187, v141, vcc
	v_cmp_lt_u32_e32 vcc, s41, v112
	v_add_u32_e32 v112, 33, v198
	s_nop 0
	v_cndmask_b32_e32 v109, v187, v109, vcc
	v_cmp_lt_u32_e32 vcc, s41, v112
	v_add_u32_e32 v112, 1, v198
	s_nop 0
	v_cndmask_b32_e32 v142, v187, v142, vcc
	v_cmp_lt_u32_e32 vcc, s41, v112
	v_add_u32_e32 v112, 32, v198
	s_nop 0
	v_cndmask_b32_e32 v110, v187, v110, vcc
	v_cmp_lt_u32_e32 vcc, s41, v112
	s_nop 1
	v_cndmask_b32_e32 v143, v187, v143, vcc
	v_cmp_lt_u32_e32 vcc, s41, v198
	s_nop 1
	v_cndmask_b32_e32 v111, v187, v111, vcc

; #define LAS __attribute__((address_space(3)))
; __device__ __forceinline__ cgptr cuni(const void* p) { const unsigned long long v = (unsigned long long)p; const unsigned lo = __builtin_amdgcn_readfirstlane((unsigned)v), hi = __builtin_amdgcn_readfirstlane((unsigned)(v >> 32)); return (cgptr)(((unsigned long long)hi << 32) | lo); }
; #define CONV_LOAD(v, c) do { const unsigned lo_ = (unsigned)(lane >> 3) * (c).N4 + 16u * (unsigned)(lane & 7); _Pragma("unroll") for (int i = 0; i < 16; ++i) v[i] = __builtin_nontemporal_load((const GAS f32x4*)(cuni((const void*)((c).src + (size_t)(8 * i) * (c).N4)) + lo_)); } while (0)
; __device__ __forceinline__ ConvItem conv_decode(int it, const float* wgu, const float* wd, unsigned char* WguT, unsigned char* WdT) {
;     constexpr int I_GU = NE * 16 * 128;
;     ConvItem c; int r = it, nbn, N; const float* src; unsigned char* dstp; bool gu;
;     if (r < I_GU) { const int e = r / (16 * 128); r -= e * (16 * 128); N = 4096; nbn = 128; src = wgu + (size_t)e * DM * 4096; dstp = WguT + (size_t)e * 4096 * DM; gu = true; }
;     else { r -= I_GU; const int e = r / (16 * 64); r -= e * (16 * 64); N = DM; nbn = 64; src = wd + (size_t)e * DFF * DM; dstp = WdT + (size_t)e * DM * DFF; gu = false; }
;     const int kb = r / nbn, nb = r - kb * nbn, n0 = nb * 32, k0 = kb * 128; int dst = n0;
;     if (gu) { const int j = n0 & 2047; dst = (j >> 7) * 256 + (j & 127) + ((n0 >= 2048) ? 128 : 0); }
;     c.src = cuni(src + (size_t)k0 * N + n0); c.dstp = cuni(dstp + (size_t)dst * DM + k0); c.N4 = (unsigned)N * 4u;
;     return c;
; }
; __device__ __forceinline__ void convert_expert_weights(const float* wgu, const float* wd, unsigned char* WguT, unsigned char* WdT, LAS float* scr, int gw, int NGW, int NIT, int lane) {
;     int it = gw; if (it >= NIT) return;
;     f32x4 va[16], vb[16];
;     ConvItem ca = conv_decode(it, wgu, wd, WguT, WdT), cb = ca;
;     CONV_LOAD(va, ca);
;     for (;;) {
;         const bool hb = it + NGW < NIT; cb = conv_decode(hb ? it + NGW : it, wgu, wd, WguT, WdT); CONV_LOAD(vb, cb);
;         CONV_STORE(va, ca);
;         if (!hb) break;
;         it += NGW;
;         const bool ha = it + NGW < NIT; ca = conv_decode(ha ? it + NGW : it, wgu, wd, WguT, WdT); CONV_LOAD(va, ca);
;         CONV_STORE(vb, cb);
;         if (!ha) break;
;         it += NGW;
;     }
.LBB0_764:
	v_cvt_f32_ubyte0_e32 v64, s9
	v_rcp_iflag_f32_e32 v64, v64
	s_sub_i32 s12, 0, s9
	s_abs_i32 s11, s8
	s_ashr_i32 s10, s8, 31
	v_mul_f32_e32 v64, 0x4f7ffffe, v64
	v_cvt_u32_f32_e32 v64, v64
	v_add_u32_e32 v152, 0x400, v148
	v_add_u32_e32 v153, 0x400, v149
	v_add_u32_e32 v154, 0x400, v150
	v_readfirstlane_b32 s17, v64
	s_mul_i32 s12, s12, s17
	s_mul_hi_u32 s12, s17, s12
	s_add_i32 s17, s17, s12
	s_mul_hi_u32 s12, s11, s17
	s_mul_i32 s17, s12, s9
	s_sub_i32 s11, s11, s17
	s_add_i32 s26, s12, 1
	s_sub_i32 s17, s11, s9
	s_cmp_ge_u32 s11, s9
	s_cselect_b32 s12, s26, s12
	s_cselect_b32 s11, s17, s11
	s_add_i32 s17, s12, 1
	s_cmp_ge_u32 s11, s9
	s_cselect_b32 s11, s17, s12
	s_xor_b32 s11, s11, s10
	s_sub_i32 s17, s11, s10
	s_mul_i32 s9, s17, s9
	s_sub_i32 s9, s8, s9
	s_lshl_b32 s12, s8, 6
	s_lshl_b32 s8, s9, 5
	s_and_b32 s10, s12, 0xf00
	s_and_b32 s11, s8, 0x60
	s_or_b32 s10, s11, s10
	s_cmp_gt_i32 s9, 63
	s_cselect_b32 s9, 0x80, 0
	s_or_b32 s9, s10, s9
	s_and_b64 s[10:11], s[18:19], exec
	s_cselect_b32 s10, s9, s8
	s_lshl_b32 s12, s17, 7
	s_mul_hi_i32 s19, s12, s3
	s_mul_i32 s18, s12, s3
	s_ashr_i32 s17, s12, 31
	s_lshl_b64 s[18:19], s[18:19], 2
	s_add_u32 s11, s24, s18
	s_addc_u32 s18, s25, s19
	s_ashr_i32 s9, s8, 31
	s_lshl_b64 s[8:9], s[8:9], 2
	s_add_u32 s24, s11, s8
	s_addc_u32 s25, s18, s9
	s_ashr_i32 s11, s10, 31
	s_lshl_b64 s[8:9], s[10:11], 11
	s_add_u32 s8, s22, s8
	s_addc_u32 s9, s23, s9
	s_add_u32 s18, s8, s12
	s_addc_u32 s19, s9, s17
	v_mul_lo_u32 v64, v130, s3
	s_lshl_b32 s8, s3, 5
	v_or_b32_e32 v64, v64, v131
	s_add_u32 s8, s24, s8
	s_addc_u32 s9, s25, 0
	global_load_dwordx4 v[124:127], v64, s[24:25] nt
	global_load_dwordx4 v[116:119], v64, s[8:9] nt
	s_lshl_b32 s8, s3, 6
	s_add_u32 s8, s24, s8
	s_addc_u32 s9, s25, 0
	s_mul_i32 s10, s3, 0x60
	s_add_u32 s10, s24, s10
	s_addc_u32 s11, s25, 0
	global_load_dwordx4 v[120:123], v64, s[8:9] nt
	global_load_dwordx4 v[108:111], v64, s[10:11] nt
	s_lshl_b32 s8, s3, 7
	s_add_u32 s8, s24, s8
	s_addc_u32 s9, s25, 0
	s_mul_i32 s10, s3, 0xa0
	s_add_u32 s10, s24, s10
	s_addc_u32 s11, s25, 0
	global_load_dwordx4 v[112:115], v64, s[8:9] nt
	global_load_dwordx4 v[100:103], v64, s[10:11] nt
	s_mul_i32 s8, s3, 0xc0
	s_add_u32 s8, s24, s8
	s_addc_u32 s9, s25, 0
	s_mul_i32 s10, s3, 0xe0
	s_add_u32 s10, s24, s10
	s_addc_u32 s11, s25, 0
	global_load_dwordx4 v[104:107], v64, s[8:9] nt
	global_load_dwordx4 v[92:95], v64, s[10:11] nt
	s_lshl_b32 s8, s3, 8
	s_add_u32 s8, s24, s8
	s_addc_u32 s9, s25, 0
	s_mul_i32 s10, s3, 0x120
	s_add_u32 s10, s24, s10
	s_addc_u32 s11, s25, 0
	global_load_dwordx4 v[96:99], v64, s[8:9] nt
	global_load_dwordx4 v[84:87], v64, s[10:11] nt
	s_mul_i32 s8, s3, 0x140
	s_add_u32 s8, s24, s8
	s_addc_u32 s9, s25, 0
	s_mul_i32 s10, s3, 0x160
	s_add_u32 s10, s24, s10
	s_addc_u32 s11, s25, 0
	global_load_dwordx4 v[88:91], v64, s[8:9] nt
	global_load_dwordx4 v[76:79], v64, s[10:11] nt
	s_mul_i32 s8, s3, 0x180
	s_add_u32 s8, s24, s8
	s_addc_u32 s9, s25, 0
	s_mul_i32 s10, s3, 0x1a0
	s_add_u32 s10, s24, s10
	s_addc_u32 s11, s25, 0
	global_load_dwordx4 v[80:83], v64, s[8:9] nt
	global_load_dwordx4 v[68:71], v64, s[10:11] nt
	s_mul_i32 s8, s3, 0x1c0
	s_add_u32 s8, s24, s8
	s_addc_u32 s9, s25, 0
	s_mulk_i32 s3, 0x1e0
	s_add_u32 s10, s24, s3
	s_waitcnt vmcnt(29)
	v_pk_mul_f32 v[6:7], v[6:7], s[16:17] op_sel_hi:[1,0]
	v_pk_mul_f32 v[4:5], v[4:5], s[16:17] op_sel_hi:[1,0]
	s_waitcnt vmcnt(28)
	v_pk_mul_f32 v[2:3], v[2:3], s[16:17] op_sel_hi:[1,0]
	v_pk_mul_f32 v[0:1], v[0:1], s[16:17] op_sel_hi:[1,0]
	s_addc_u32 s11, s25, 0
	global_load_dwordx4 v[72:75], v64, s[8:9] nt
	s_nop 0
	global_load_dwordx4 v[64:67], v64, s[10:11] nt
	ds_write_b128 v132, v[4:7]
	ds_write_b128 v133, v[0:3]
	s_waitcnt vmcnt(29)
	v_pk_mul_f32 v[2:3], v[14:15], s[16:17] op_sel_hi:[1,0]
	v_pk_mul_f32 v[0:1], v[12:13], s[16:17] op_sel_hi:[1,0]
	ds_write_b128 v134, v[0:3]
	s_waitcnt vmcnt(28)
	v_pk_mul_f32 v[2:3], v[10:11], s[16:17] op_sel_hi:[1,0]
	v_pk_mul_f32 v[0:1], v[8:9], s[16:17] op_sel_hi:[1,0]
	ds_write_b128 v135, v[0:3]
	s_waitcnt vmcnt(27)
	v_pk_mul_f32 v[2:3], v[22:23], s[16:17] op_sel_hi:[1,0]
	v_pk_mul_f32 v[0:1], v[20:21], s[16:17] op_sel_hi:[1,0]
	ds_write_b128 v136, v[0:3]
	s_waitcnt vmcnt(26)
	v_pk_mul_f32 v[2:3], v[18:19], s[16:17] op_sel_hi:[1,0]
	v_pk_mul_f32 v[0:1], v[16:17], s[16:17] op_sel_hi:[1,0]
	ds_write_b128 v137, v[0:3]
	s_waitcnt vmcnt(25)
	v_pk_mul_f32 v[2:3], v[30:31], s[16:17] op_sel_hi:[1,0]
	v_pk_mul_f32 v[0:1], v[28:29], s[16:17] op_sel_hi:[1,0]
	ds_write_b128 v138, v[0:3]
	s_waitcnt vmcnt(24)
	v_pk_mul_f32 v[2:3], v[26:27], s[16:17] op_sel_hi:[1,0]
	v_pk_mul_f32 v[0:1], v[24:25], s[16:17] op_sel_hi:[1,0]
	ds_write_b128 v139, v[0:3]
	s_waitcnt vmcnt(23)
	v_pk_mul_f32 v[2:3], v[38:39], s[16:17] op_sel_hi:[1,0]
	v_pk_mul_f32 v[0:1], v[36:37], s[16:17] op_sel_hi:[1,0]
	ds_write_b128 v140, v[0:3]
	s_waitcnt vmcnt(22)
	v_pk_mul_f32 v[2:3], v[34:35], s[16:17] op_sel_hi:[1,0]
	v_pk_mul_f32 v[0:1], v[32:33], s[16:17] op_sel_hi:[1,0]
	ds_write_b128 v141, v[0:3]
	s_waitcnt vmcnt(21)
	v_pk_mul_f32 v[2:3], v[46:47], s[16:17] op_sel_hi:[1,0]
	v_pk_mul_f32 v[0:1], v[44:45], s[16:17] op_sel_hi:[1,0]
	ds_write_b128 v142, v[0:3]
	s_waitcnt vmcnt(20)
; __device__ __forceinline__ ConvItem conv_decode(int it, const float* wgu, const float* wd, unsigned char* WguT, unsigned char* WdT) {
;     constexpr int I_GU = NE * 16 * 128;
;     ConvItem c; int r = it, nbn, N; const float* src; unsigned char* dstp; bool gu;
;     if (r < I_GU) { const int e = r / (16 * 128); r -= e * (16 * 128); N = 4096; nbn = 128; src = wgu + (size_t)e * DM * 4096; dstp = WguT + (size_t)e * 4096 * DM; gu = true; }
;     else { r -= I_GU; const int e = r / (16 * 64); r -= e * (16 * 64); N = DM; nbn = 64; src = wd + (size_t)e * DFF * DM; dstp = WdT + (size_t)e * DM * DFF; gu = false; }
;     const int kb = r / nbn, nb = r - kb * nbn, n0 = nb * 32, k0 = kb * 128; int dst = n0;
;     if (gu) { const int j = n0 & 2047; dst = (j >> 7) * 256 + (j & 127) + ((n0 >= 2048) ? 128 : 0); }
	v_pk_mul_f32 v[2:3], v[42:43], s[16:17] op_sel_hi:[1,0]
	v_pk_mul_f32 v[0:1], v[40:41], s[16:17] op_sel_hi:[1,0]
	ds_write_b128 v143, v[0:3]
	s_waitcnt vmcnt(19)
	v_pk_mul_f32 v[2:3], v[54:55], s[16:17] op_sel_hi:[1,0]
	v_pk_mul_f32 v[0:1], v[52:53], s[16:17] op_sel_hi:[1,0]
	ds_write_b128 v144, v[0:3]
	s_waitcnt vmcnt(18)
	v_pk_mul_f32 v[2:3], v[50:51], s[16:17] op_sel_hi:[1,0]
	v_pk_mul_f32 v[0:1], v[48:49], s[16:17] op_sel_hi:[1,0]
	ds_write_b128 v145, v[0:3]
	s_waitcnt vmcnt(17)
	v_pk_mul_f32 v[2:3], v[62:63], s[16:17] op_sel_hi:[1,0]
	v_pk_mul_f32 v[0:1], v[60:61], s[16:17] op_sel_hi:[1,0]
	ds_write_b128 v146, v[0:3]
	s_waitcnt vmcnt(16)
	v_pk_mul_f32 v[2:3], v[58:59], s[16:17] op_sel_hi:[1,0]
	v_pk_mul_f32 v[0:1], v[56:57], s[16:17] op_sel_hi:[1,0]
	ds_write_b128 v147, v[0:3]
	s_waitcnt lgkmcnt(0)
	ds_read2_b32 v[0:1], v148 offset1:32
	ds_read2_b32 v[8:9], v148 offset0:64 offset1:96
	s_add_u32 s8, s14, 0x4000
	s_waitcnt lgkmcnt(0)
	v_cvt_pk_fp8_f32 v4, v0, v1
	ds_read2_b32 v[0:1], v148 offset0:128 offset1:160
	ds_read2_b32 v[10:11], v148 offset0:192 offset1:224
	ds_read2_b32 v[12:13], v152 offset1:32
	s_waitcnt lgkmcnt(2)
	v_cvt_pk_fp8_f32 v5, v0, v1
	ds_read2_b32 v[0:1], v152 offset0:64 offset1:96
	ds_read2_b32 v[14:15], v152 offset0:128 offset1:160
	s_waitcnt lgkmcnt(2)
	v_cvt_pk_fp8_f32 v6, v12, v13
	ds_read2_b32 v[12:13], v152 offset0:192 offset1:224
	v_cvt_pk_fp8_f32 v4, v8, v9 op_sel:[0,0,1]
	s_waitcnt lgkmcnt(1)
	v_cvt_pk_fp8_f32 v7, v14, v15
	v_cvt_pk_fp8_f32 v5, v10, v11 op_sel:[0,0,1]
	v_cvt_pk_fp8_f32 v6, v0, v1 op_sel:[0,0,1]
	ds_read2_b32 v[0:1], v149 offset1:32
	s_waitcnt lgkmcnt(1)
	v_cvt_pk_fp8_f32 v7, v12, v13 op_sel:[0,0,1]
	v_lshl_add_u64 v[8:9], s[14:15], 0, v[128:129]
	s_addc_u32 s9, s15, 0
	v_add_u32_e32 v155, 0x400, v151
	global_store_dwordx4 v[8:9], v[4:7], off nt
	ds_read2_b32 v[8:9], v149 offset0:64 offset1:96
	s_waitcnt lgkmcnt(1)
	v_cvt_pk_fp8_f32 v4, v0, v1
	ds_read2_b32 v[0:1], v149 offset0:128 offset1:160
	ds_read2_b32 v[10:11], v149 offset0:192 offset1:224
	ds_read2_b32 v[12:13], v153 offset1:32
	s_waitcnt lgkmcnt(2)
	v_cvt_pk_fp8_f32 v5, v0, v1
	ds_read2_b32 v[0:1], v153 offset0:64 offset1:96
	ds_read2_b32 v[14:15], v153 offset0:128 offset1:160
	s_waitcnt lgkmcnt(2)
	v_cvt_pk_fp8_f32 v6, v12, v13
	ds_read2_b32 v[12:13], v153 offset0:192 offset1:224
	v_cvt_pk_fp8_f32 v4, v8, v9 op_sel:[0,0,1]
	s_waitcnt lgkmcnt(1)
	v_cvt_pk_fp8_f32 v7, v14, v15
	v_cvt_pk_fp8_f32 v5, v10, v11 op_sel:[0,0,1]
	v_cvt_pk_fp8_f32 v6, v0, v1 op_sel:[0,0,1]
	ds_read2_b32 v[0:1], v150 offset1:32
	s_waitcnt lgkmcnt(1)
	v_cvt_pk_fp8_f32 v7, v12, v13 op_sel:[0,0,1]
	v_lshl_add_u64 v[8:9], s[8:9], 0, v[128:129]
	s_add_u32 s8, s14, 0x8000
	s_addc_u32 s9, s15, 0
	global_store_dwordx4 v[8:9], v[4:7], off nt
	ds_read2_b32 v[8:9], v150 offset0:64 offset1:96
	s_nop 0
	s_waitcnt lgkmcnt(1)
	v_cvt_pk_fp8_f32 v4, v0, v1
	ds_read2_b32 v[0:1], v150 offset0:128 offset1:160
	ds_read2_b32 v[10:11], v150 offset0:192 offset1:224
	ds_read2_b32 v[12:13], v154 offset1:32
	s_waitcnt lgkmcnt(2)
	v_cvt_pk_fp8_f32 v5, v0, v1
	ds_read2_b32 v[0:1], v154 offset0:64 offset1:96
	ds_read2_b32 v[14:15], v154 offset0:128 offset1:160
	s_waitcnt lgkmcnt(2)
	v_cvt_pk_fp8_f32 v6, v12, v13
	ds_read2_b32 v[12:13], v154 offset0:192 offset1:224
	v_cvt_pk_fp8_f32 v4, v8, v9 op_sel:[0,0,1]
	s_waitcnt lgkmcnt(1)
	v_cvt_pk_fp8_f32 v7, v14, v15
	v_cvt_pk_fp8_f32 v5, v10, v11 op_sel:[0,0,1]
	v_cvt_pk_fp8_f32 v6, v0, v1 op_sel:[0,0,1]
	ds_read2_b32 v[8:9], v151 offset1:32
	s_waitcnt lgkmcnt(1)
	v_cvt_pk_fp8_f32 v7, v12, v13 op_sel:[0,0,1]
	v_lshl_add_u64 v[0:1], s[8:9], 0, v[128:129]
	s_add_u32 s8, s14, 0xc000
	s_addc_u32 s9, s15, 0
	global_store_dwordx4 v[0:1], v[4:7], off nt
	ds_read2_b32 v[4:5], v151 offset0:64 offset1:96
	s_waitcnt lgkmcnt(1)
	v_cvt_pk_fp8_f32 v0, v8, v9
	ds_read2_b32 v[6:7], v151 offset0:128 offset1:160
	ds_read2_b32 v[8:9], v151 offset0:192 offset1:224
	ds_read2_b32 v[10:11], v155 offset1:32
	s_waitcnt lgkmcnt(3)
	v_cvt_pk_fp8_f32 v0, v4, v5 op_sel:[0,0,1]
	s_waitcnt lgkmcnt(2)
	v_cvt_pk_fp8_f32 v1, v6, v7
	ds_read2_b32 v[6:7], v155 offset0:128 offset1:160
	ds_read2_b32 v[12:13], v155 offset0:64 offset1:96
	s_waitcnt lgkmcnt(2)
	v_cvt_pk_fp8_f32 v2, v10, v11
	ds_read2_b32 v[10:11], v155 offset0:192 offset1:224
	v_cvt_pk_fp8_f32 v1, v8, v9 op_sel:[0,0,1]
	s_waitcnt lgkmcnt(2)
	v_cvt_pk_fp8_f32 v3, v6, v7
	s_waitcnt lgkmcnt(1)
	v_cvt_pk_fp8_f32 v2, v12, v13 op_sel:[0,0,1]
	v_lshl_add_u64 v[4:5], s[8:9], 0, v[128:129]
	s_andn2_b64 vcc, exec, s[20:21]
	s_waitcnt lgkmcnt(0)
	v_cvt_pk_fp8_f32 v3, v10, v11 op_sel:[0,0,1]
	s_mov_b64 s[20:21], -1
	global_store_dwordx4 v[4:5], v[0:3], off nt
	s_waitcnt lgkmcnt(0)
	s_cbranch_vccnz .LBB0_758
	s_add_i32 s3, s0, s38
	s_cmp_lt_i32 s3, s45
	s_cselect_b32 s3, s3, s1
	s_cmp_lt_i32 s3, 0x10000
	s_cselect_b64 s[14:15], -1, 0
	s_cmp_gt_i32 s3, 0xffff
	s_mov_b64 s[24:25], -1
	s_cbranch_scc0 .LBB0_767
	s_add_i32 s8, s3, 0xffff0000
	s_lshr_b32 s12, s8, 10
	s_and_b32 s8, s3, 0x3ff
	s_lshl_b64 s[10:11], s[12:13], 22
	s_lshl_b64 s[20:21], s[12:13], 24
	s_add_u32 s22, s6, s20
	s_addc_u32 s23, s7, s21
	s_add_u32 s20, s77, s10
	v_readlane_b32 s9, v252, 33
	s_addc_u32 s21, s9, s11
	s_mov_b64 s[24:25], 0

; __global__ void __launch_bounds__(512, 2) fwd_kernel(Params p) {
	.amdhsa_kernel _Z10fwd_kernel6Params
		.amdhsa_group_segment_fixed_size 0
		.amdhsa_private_segment_fixed_size 0
		.amdhsa_kernarg_size 456
		.amdhsa_user_sgpr_count 2
		.amdhsa_user_sgpr_dispatch_ptr 0
		.amdhsa_user_sgpr_queue_ptr 0
		.amdhsa_user_sgpr_kernarg_segment_ptr 1
		.amdhsa_user_sgpr_dispatch_id 0
		.amdhsa_user_sgpr_kernarg_preload_length 0
		.amdhsa_user_sgpr_kernarg_preload_offset 0
		.amdhsa_user_sgpr_private_segment_size 0
		.amdhsa_uses_dynamic_stack 0
		.amdhsa_enable_private_segment 0
		.amdhsa_system_sgpr_workgroup_id_x 1
		.amdhsa_system_sgpr_workgroup_id_y 0
		.amdhsa_system_sgpr_workgroup_id_z 0
		.amdhsa_system_sgpr_workgroup_info 0
		.amdhsa_system_vgpr_workitem_id 0
		.amdhsa_next_free_vgpr 256
		.amdhsa_next_free_sgpr 100
		.amdhsa_accum_offset 256
		.amdhsa_reserve_vcc 1
		.amdhsa_float_round_mode_32 0
		.amdhsa_float_round_mode_16_64 0
		.amdhsa_float_denorm_mode_32 3
		.amdhsa_float_denorm_mode_16_64 3
		.amdhsa_dx10_clamp 1
		.amdhsa_ieee_mode 1
		.amdhsa_fp16_overflow 0
		.amdhsa_tg_split 0
		.amdhsa_exception_fp_ieee_invalid_op 0
		.amdhsa_exception_fp_denorm_src 0
		.amdhsa_exception_fp_ieee_div_zero 0
		.amdhsa_exception_fp_ieee_overflow 0
		.amdhsa_exception_fp_ieee_underflow 0
		.amdhsa_exception_fp_ieee_inexact 0
		.amdhsa_exception_int_div_zero 0
	.end_amdhsa_kernel

; __global__ void __launch_bounds__(512, 2) fwd_kernel(Params p) {
amdhsa.kernels:
  - .agpr_count:     0
    .args:
      - .offset:         0
        .size:           200
        .value_kind:     by_value
      - .offset:         200
        .size:           4
        .value_kind:     hidden_block_count_x
      - .offset:         204
        .size:           4
        .value_kind:     hidden_block_count_y
      - .offset:         208
        .size:           4
        .value_kind:     hidden_block_count_z
      - .offset:         212
        .size:           2
        .value_kind:     hidden_group_size_x
      - .offset:         214
        .size:           2
        .value_kind:     hidden_group_size_y
      - .offset:         216
        .size:           2
        .value_kind:     hidden_group_size_z
      - .offset:         218
        .size:           2
        .value_kind:     hidden_remainder_x
      - .offset:         220
        .size:           2
        .value_kind:     hidden_remainder_y
      - .offset:         222
        .size:           2
        .value_kind:     hidden_remainder_z
      - .offset:         240
        .size:           8
        .value_kind:     hidden_global_offset_x
      - .offset:         248
        .size:           8
        .value_kind:     hidden_global_offset_y
      - .offset:         256
        .size:           8
        .value_kind:     hidden_global_offset_z
      - .offset:         264
        .size:           2
        .value_kind:     hidden_grid_dims
      - .offset:         320
        .size:           4
        .value_kind:     hidden_dynamic_lds_size
    .group_segment_fixed_size: 0
    .kernarg_segment_align: 8
    .kernarg_segment_size: 456
    .language:       OpenCL C
    .language_version:
      - 2
      - 0
    .max_flat_workgroup_size: 512
    .name:           _Z10fwd_kernel6Params
    .private_segment_fixed_size: 0
    .sgpr_count:     106
    .sgpr_spill_count: 46
    .symbol:         _Z10fwd_kernel6Params.kd
    .uniform_work_group_size: 1
    .uses_dynamic_stack: false
    .vgpr_count:     256
    .vgpr_spill_count: 0
    .wavefront_size: 64
